# combination of the individually neutral edits (EpiGate2 mid batching, cvt 32-deep + nt, DPP reductions, attention back-edge rotation, A4 KV CU rotation, A8 last-layer stagger skip) on top of v040
# baseline (speedup 1.0000x reference)
.LBB0_57:
	s_lshl_b32 s27, s8, 1
	s_lshl_b32 s30, s20, 1
	v_or_b32_e32 v21, s27, v1
	v_or_b32_e32 v31, s30, v6
	s_add_i32 s31, s27, 4
	s_add_i32 s41, s30, 4
	s_add_i32 s49, s27, 8
	s_add_i32 s50, s30, 8
	s_add_i32 s51, s27, 12
	s_add_i32 s52, s30, 12
	s_add_i32 s53, s27, 16
	s_add_i32 s54, s30, 16
	s_add_i32 s55, s27, 20
	s_add_i32 s56, s30, 20
	s_add_i32 s57, s27, 24
	s_add_i32 s58, s30, 24
	s_add_i32 s27, s27, 28
	s_add_i32 s30, s30, 28
	v_add_u32_e32 v33, s5, v21
	v_add_u32_e32 v4, s26, v31
	v_or_b32_e32 v35, s31, v1
	v_or_b32_e32 v37, s41, v6
	v_or_b32_e32 v39, s49, v1
	v_or_b32_e32 v41, s50, v6
	v_or_b32_e32 v43, s51, v1
	v_or_b32_e32 v47, s52, v6
	v_or_b32_e32 v49, s53, v1
	v_or_b32_e32 v51, s54, v6
	v_or_b32_e32 v53, s55, v1
	v_or_b32_e32 v88, s56, v6
	v_or_b32_e32 v89, s57, v1
	v_or_b32_e32 v90, s58, v6
	v_or_b32_e32 v91, s27, v1
	v_or_b32_e32 v92, s30, v6
	v_mad_i64_i32 v[4:5], s[30:31], v4, s44, v[2:3]
	v_mad_i64_i32 v[54:55], s[30:31], v33, s44, v[2:3]
	v_add_u32_e32 v33, s5, v35
	v_add_u32_e32 v56, s26, v37
	v_add_u32_e32 v66, s5, v39
	v_add_u32_e32 v64, s26, v41
	v_add_u32_e32 v70, s5, v43
	v_add_u32_e32 v68, s26, v47
	v_add_u32_e32 v74, s5, v49
	v_add_u32_e32 v72, s26, v51
	v_add_u32_e32 v78, s5, v53
	v_add_u32_e32 v76, s26, v88
	v_add_u32_e32 v82, s5, v89
	v_add_u32_e32 v80, s26, v90
	v_add_u32_e32 v86, s5, v91
	v_add_u32_e32 v84, s26, v92
	v_mad_i64_i32 v[56:57], s[30:31], v56, s44, v[2:3]
	v_mad_i64_i32 v[58:59], s[30:31], v33, s44, v[2:3]
	v_mad_i64_i32 v[64:65], s[30:31], v64, s44, v[2:3]
	v_mad_i64_i32 v[66:67], s[30:31], v66, s44, v[2:3]
	v_mad_i64_i32 v[68:69], s[30:31], v68, s44, v[2:3]
	v_mad_i64_i32 v[70:71], s[30:31], v70, s44, v[2:3]
	v_mad_i64_i32 v[72:73], s[30:31], v72, s44, v[2:3]
	v_mad_i64_i32 v[74:75], s[30:31], v74, s44, v[2:3]
	v_mad_i64_i32 v[76:77], s[30:31], v76, s44, v[2:3]
	v_mad_i64_i32 v[78:79], s[30:31], v78, s44, v[2:3]
	v_mad_i64_i32 v[80:81], s[30:31], v80, s44, v[2:3]
	v_mad_i64_i32 v[82:83], s[30:31], v82, s44, v[2:3]
	v_mad_i64_i32 v[84:85], s[30:31], v84, s44, v[2:3]
	v_mad_i64_i32 v[86:87], s[30:31], v86, s44, v[2:3]
	global_load_dword v33, v[4:5], off nt
	global_load_dword v93, v[54:55], off nt
	global_load_dword v94, v[56:57], off nt
	global_load_dword v95, v[58:59], off nt
	global_load_dword v96, v[64:65], off nt
	global_load_dword v97, v[66:67], off nt
	global_load_dword v98, v[68:69], off nt
	global_load_dword v99, v[70:71], off nt
	global_load_dword v100, v[72:73], off nt
	global_load_dword v101, v[74:75], off nt
	global_load_dword v102, v[76:77], off nt
	global_load_dword v103, v[78:79], off nt
	global_load_dword v104, v[80:81], off nt
	global_load_dword v105, v[82:83], off nt
	global_load_dword v106, v[84:85], off nt
	global_load_dword v107, v[86:87], off nt
	s_add_i32 s20, s20, 16
	s_add_i32 s8, s8, 16
	s_add_i32 s21, s21, -16
	v_mad_u64_u32 v[4:5], s[30:31], v31, s43, v[10:11]
	s_cmp_lg_u32 s21, 0
	v_mad_u64_u32 v[54:55], s[30:31], v21, s43, v[10:11]
	v_mad_u64_u32 v[56:57], s[30:31], v37, s43, v[10:11]
	v_mad_u64_u32 v[58:59], s[30:31], v35, s43, v[10:11]
	v_mad_u64_u32 v[64:65], s[30:31], v41, s43, v[10:11]
	v_mad_u64_u32 v[66:67], s[30:31], v39, s43, v[10:11]
	v_mad_u64_u32 v[68:69], s[30:31], v47, s43, v[10:11]
	v_mad_u64_u32 v[70:71], s[30:31], v43, s43, v[10:11]
	v_mad_u64_u32 v[72:73], s[30:31], v51, s43, v[10:11]
	v_mad_u64_u32 v[74:75], s[30:31], v49, s43, v[10:11]
	v_mad_u64_u32 v[76:77], s[30:31], v88, s43, v[10:11]
	v_mad_u64_u32 v[78:79], s[30:31], v53, s43, v[10:11]
	v_mad_u64_u32 v[80:81], s[30:31], v90, s43, v[10:11]
	v_mad_u64_u32 v[82:83], s[30:31], v89, s43, v[10:11]
	v_mad_u64_u32 v[84:85], s[30:31], v92, s43, v[10:11]
	v_mad_u64_u32 v[86:87], s[30:31], v91, s43, v[10:11]
	s_lshl_b32 s27, s8, 1
	s_lshl_b32 s30, s20, 1
	v_or_b32_e32 v112, s27, v1
	v_or_b32_e32 v113, s30, v6
	s_add_i32 s31, s27, 4
	s_add_i32 s41, s30, 4
	s_add_i32 s49, s27, 8
	s_add_i32 s50, s30, 8
	s_add_i32 s51, s27, 12
	s_add_i32 s52, s30, 12
	s_add_i32 s53, s27, 16
	s_add_i32 s54, s30, 16
	s_add_i32 s55, s27, 20
	s_add_i32 s56, s30, 20
	s_add_i32 s57, s27, 24
	s_add_i32 s58, s30, 24
	s_add_i32 s27, s27, 28
	s_add_i32 s30, s30, 28
	v_add_u32_e32 v114, s5, v112
	v_add_u32_e32 v110, s26, v113
	v_or_b32_e32 v115, s31, v1
	v_or_b32_e32 v116, s41, v6
	v_or_b32_e32 v117, s49, v1
	v_or_b32_e32 v118, s50, v6
	v_or_b32_e32 v119, s51, v1
	v_or_b32_e32 v120, s52, v6
	v_or_b32_e32 v121, s53, v1
	v_or_b32_e32 v122, s54, v6
	v_or_b32_e32 v123, s55, v1
	v_or_b32_e32 v154, s56, v6
	v_or_b32_e32 v155, s57, v1
	v_or_b32_e32 v156, s58, v6
	v_or_b32_e32 v157, s27, v1
	v_or_b32_e32 v158, s30, v6
	v_mad_i64_i32 v[110:111], s[30:31], v110, s44, v[2:3]
	v_mad_i64_i32 v[124:125], s[30:31], v114, s44, v[2:3]
	v_add_u32_e32 v114, s5, v115
	v_add_u32_e32 v126, s26, v116
	v_add_u32_e32 v132, s5, v117
	v_add_u32_e32 v130, s26, v118
	v_add_u32_e32 v136, s5, v119
	v_add_u32_e32 v134, s26, v120
	v_add_u32_e32 v140, s5, v121
	v_add_u32_e32 v138, s26, v122
	v_add_u32_e32 v144, s5, v123
	v_add_u32_e32 v142, s26, v154
	v_add_u32_e32 v148, s5, v155
	v_add_u32_e32 v146, s26, v156
	v_add_u32_e32 v152, s5, v157
	v_add_u32_e32 v150, s26, v158
	v_mad_i64_i32 v[126:127], s[30:31], v126, s44, v[2:3]
	v_mad_i64_i32 v[128:129], s[30:31], v114, s44, v[2:3]
	v_mad_i64_i32 v[130:131], s[30:31], v130, s44, v[2:3]
	v_mad_i64_i32 v[132:133], s[30:31], v132, s44, v[2:3]
	v_mad_i64_i32 v[134:135], s[30:31], v134, s44, v[2:3]
	v_mad_i64_i32 v[136:137], s[30:31], v136, s44, v[2:3]
	v_mad_i64_i32 v[138:139], s[30:31], v138, s44, v[2:3]
	v_mad_i64_i32 v[140:141], s[30:31], v140, s44, v[2:3]
	v_mad_i64_i32 v[142:143], s[30:31], v142, s44, v[2:3]
	v_mad_i64_i32 v[144:145], s[30:31], v144, s44, v[2:3]
	v_mad_i64_i32 v[146:147], s[30:31], v146, s44, v[2:3]
	v_mad_i64_i32 v[148:149], s[30:31], v148, s44, v[2:3]
	v_mad_i64_i32 v[150:151], s[30:31], v150, s44, v[2:3]
	v_mad_i64_i32 v[152:153], s[30:31], v152, s44, v[2:3]
	global_load_dword v114, v[110:111], off nt
	global_load_dword v159, v[124:125], off nt
	global_load_dword v160, v[126:127], off nt
	global_load_dword v161, v[128:129], off nt
	global_load_dword v162, v[130:131], off nt
	global_load_dword v163, v[132:133], off nt
	global_load_dword v164, v[134:135], off nt
	global_load_dword v165, v[136:137], off nt
	global_load_dword v166, v[138:139], off nt
	global_load_dword v167, v[140:141], off nt
	global_load_dword v168, v[142:143], off nt
	global_load_dword v169, v[144:145], off nt
	global_load_dword v170, v[146:147], off nt
	global_load_dword v171, v[148:149], off nt
	global_load_dword v172, v[150:151], off nt
	global_load_dword v173, v[152:153], off nt
	s_add_i32 s20, s20, 16
	s_add_i32 s8, s8, 16
	s_add_i32 s21, s21, -16
	v_mad_u64_u32 v[110:111], s[30:31], v113, s43, v[10:11]
	s_cmp_lg_u32 s21, 0
	v_mad_u64_u32 v[124:125], s[30:31], v112, s43, v[10:11]
	v_mad_u64_u32 v[126:127], s[30:31], v116, s43, v[10:11]
	v_mad_u64_u32 v[128:129], s[30:31], v115, s43, v[10:11]
	v_mad_u64_u32 v[130:131], s[30:31], v118, s43, v[10:11]
	v_mad_u64_u32 v[132:133], s[30:31], v117, s43, v[10:11]
	v_mad_u64_u32 v[134:135], s[30:31], v120, s43, v[10:11]
	v_mad_u64_u32 v[136:137], s[30:31], v119, s43, v[10:11]
	v_mad_u64_u32 v[138:139], s[30:31], v122, s43, v[10:11]
	v_mad_u64_u32 v[140:141], s[30:31], v121, s43, v[10:11]
	v_mad_u64_u32 v[142:143], s[30:31], v154, s43, v[10:11]
	v_mad_u64_u32 v[144:145], s[30:31], v123, s43, v[10:11]
	v_mad_u64_u32 v[146:147], s[30:31], v156, s43, v[10:11]
	v_mad_u64_u32 v[148:149], s[30:31], v155, s43, v[10:11]
	v_mad_u64_u32 v[150:151], s[30:31], v158, s43, v[10:11]
	v_mad_u64_u32 v[152:153], s[30:31], v157, s43, v[10:11]
	s_waitcnt vmcnt(31)
	ds_write_b32 v4, v33
	s_waitcnt vmcnt(30)
	ds_write_b32 v54, v93
	s_waitcnt vmcnt(29)
	ds_write_b32 v56, v94
	s_waitcnt vmcnt(28)
	ds_write_b32 v58, v95
	s_waitcnt vmcnt(27)
	ds_write_b32 v64, v96
	s_waitcnt vmcnt(26)
	ds_write_b32 v66, v97
	s_waitcnt vmcnt(25)
	ds_write_b32 v68, v98
	s_waitcnt vmcnt(24)
	ds_write_b32 v70, v99
	s_waitcnt vmcnt(23)
	ds_write_b32 v72, v100
	s_waitcnt vmcnt(22)
	ds_write_b32 v74, v101
	s_waitcnt vmcnt(21)
	ds_write_b32 v76, v102
	s_waitcnt vmcnt(20)
	ds_write_b32 v78, v103
	s_waitcnt vmcnt(19)
	ds_write_b32 v80, v104
	s_waitcnt vmcnt(18)
	ds_write_b32 v82, v105
	s_waitcnt vmcnt(17)
	ds_write_b32 v84, v106
	s_waitcnt vmcnt(16)
	ds_write_b32 v86, v107
	s_waitcnt vmcnt(15)
	ds_write_b32 v110, v114
	s_waitcnt vmcnt(14)
	ds_write_b32 v124, v159
	s_waitcnt vmcnt(13)
	ds_write_b32 v126, v160
	s_waitcnt vmcnt(12)
	ds_write_b32 v128, v161
	s_waitcnt vmcnt(11)
	ds_write_b32 v130, v162
	s_waitcnt vmcnt(10)
	ds_write_b32 v132, v163
	s_waitcnt vmcnt(9)
	ds_write_b32 v134, v164
	s_waitcnt vmcnt(8)
	ds_write_b32 v136, v165
	s_waitcnt vmcnt(7)
	ds_write_b32 v138, v166
	s_waitcnt vmcnt(6)
	ds_write_b32 v140, v167
	s_waitcnt vmcnt(5)
	ds_write_b32 v142, v168
	s_waitcnt vmcnt(4)
	ds_write_b32 v144, v169
	s_waitcnt vmcnt(3)
	ds_write_b32 v146, v170
	s_waitcnt vmcnt(2)
	ds_write_b32 v148, v171
	s_waitcnt vmcnt(1)
	ds_write_b32 v150, v172
	s_waitcnt vmcnt(0)
	ds_write_b32 v152, v173

.LBB0_141:
	s_lshl_b32 s38, s21, 1
	s_lshl_b32 s39, s31, 1
	v_or_b32_e32 v21, s38, v1
	v_or_b32_e32 v31, s39, v6
	s_add_i32 s40, s38, 4
	s_add_i32 s41, s39, 4
	s_add_i32 s49, s38, 8
	s_add_i32 s50, s39, 8
	s_add_i32 s51, s38, 12
	s_add_i32 s52, s39, 12
	s_add_i32 s53, s38, 16
	s_add_i32 s54, s39, 16
	s_add_i32 s55, s38, 20
	s_add_i32 s56, s39, 20
	s_add_i32 s57, s38, 24
	s_add_i32 s58, s39, 24
	s_add_i32 s38, s38, 28
	s_add_i32 s39, s39, 28
	v_add_u32_e32 v56, s34, v31
	v_or_b32_e32 v33, s40, v1
	v_or_b32_e32 v35, s41, v6
	v_or_b32_e32 v37, s49, v1
	v_or_b32_e32 v39, s50, v6
	v_or_b32_e32 v41, s51, v1
	v_or_b32_e32 v43, s52, v6
	v_or_b32_e32 v47, s53, v1
	v_or_b32_e32 v49, s54, v6
	v_or_b32_e32 v51, s55, v1
	v_or_b32_e32 v53, s56, v6
	v_or_b32_e32 v90, s57, v1
	v_or_b32_e32 v91, s58, v6
	v_or_b32_e32 v92, s38, v1
	v_or_b32_e32 v93, s39, v6
	v_add_u32_e32 v4, s20, v21
	v_ashrrev_i32_e32 v57, 31, v56
	v_add_u32_e32 v58, s20, v33
	v_add_u32_e32 v64, s34, v35
	v_add_u32_e32 v66, s20, v37
	v_add_u32_e32 v68, s34, v39
	v_add_u32_e32 v70, s20, v41
	v_add_u32_e32 v72, s34, v43
	v_add_u32_e32 v74, s20, v47
	v_add_u32_e32 v76, s34, v49
	v_add_u32_e32 v78, s20, v51
	v_add_u32_e32 v80, s34, v53
	v_add_u32_e32 v82, s20, v90
	v_add_u32_e32 v84, s34, v91
	v_add_u32_e32 v86, s20, v92
	v_add_u32_e32 v88, s34, v93
	v_ashrrev_i32_e32 v5, 31, v4
	v_lshlrev_b64 v[56:57], 12, v[56:57]
	v_ashrrev_i32_e32 v65, 31, v64
	v_ashrrev_i32_e32 v59, 31, v58
	v_ashrrev_i32_e32 v69, 31, v68
	v_ashrrev_i32_e32 v67, 31, v66
	v_ashrrev_i32_e32 v73, 31, v72
	v_ashrrev_i32_e32 v71, 31, v70
	v_ashrrev_i32_e32 v77, 31, v76
	v_ashrrev_i32_e32 v75, 31, v74
	v_ashrrev_i32_e32 v81, 31, v80
	v_ashrrev_i32_e32 v79, 31, v78
	v_ashrrev_i32_e32 v85, 31, v84
	v_ashrrev_i32_e32 v83, 31, v82
	v_ashrrev_i32_e32 v89, 31, v88
	v_ashrrev_i32_e32 v87, 31, v86
	v_lshlrev_b64 v[4:5], 12, v[4:5]
	v_lshl_add_u64 v[56:57], v[2:3], 0, v[56:57]
	v_lshlrev_b64 v[58:59], 12, v[58:59]
	v_lshlrev_b64 v[64:65], 12, v[64:65]
	v_lshlrev_b64 v[66:67], 12, v[66:67]
	v_lshlrev_b64 v[68:69], 12, v[68:69]
	v_lshlrev_b64 v[70:71], 12, v[70:71]
	v_lshlrev_b64 v[72:73], 12, v[72:73]
	v_lshlrev_b64 v[74:75], 12, v[74:75]
	v_lshlrev_b64 v[76:77], 12, v[76:77]
	v_lshlrev_b64 v[78:79], 12, v[78:79]
	v_lshlrev_b64 v[80:81], 12, v[80:81]
	v_lshlrev_b64 v[82:83], 12, v[82:83]
	v_lshlrev_b64 v[84:85], 12, v[84:85]
	v_lshlrev_b64 v[86:87], 12, v[86:87]
	v_lshlrev_b64 v[88:89], 12, v[88:89]
	v_lshl_add_u64 v[4:5], v[2:3], 0, v[4:5]
	v_lshl_add_u64 v[64:65], v[2:3], 0, v[64:65]
	v_lshl_add_u64 v[58:59], v[2:3], 0, v[58:59]
	v_lshl_add_u64 v[68:69], v[2:3], 0, v[68:69]
	v_lshl_add_u64 v[66:67], v[2:3], 0, v[66:67]
	v_lshl_add_u64 v[72:73], v[2:3], 0, v[72:73]
	v_lshl_add_u64 v[70:71], v[2:3], 0, v[70:71]
	v_lshl_add_u64 v[76:77], v[2:3], 0, v[76:77]
	v_lshl_add_u64 v[74:75], v[2:3], 0, v[74:75]
	v_lshl_add_u64 v[80:81], v[2:3], 0, v[80:81]
	v_lshl_add_u64 v[78:79], v[2:3], 0, v[78:79]
	v_lshl_add_u64 v[84:85], v[2:3], 0, v[84:85]
	v_lshl_add_u64 v[82:83], v[2:3], 0, v[82:83]
	v_lshl_add_u64 v[88:89], v[2:3], 0, v[88:89]
	v_lshl_add_u64 v[86:87], v[2:3], 0, v[86:87]
	global_load_dword v94, v[56:57], off nt
	global_load_dword v95, v[4:5], off nt
	global_load_dword v96, v[64:65], off nt
	global_load_dword v97, v[58:59], off nt
	global_load_dword v98, v[68:69], off nt
	global_load_dword v99, v[66:67], off nt
	global_load_dword v100, v[72:73], off nt
	global_load_dword v101, v[70:71], off nt
	global_load_dword v102, v[76:77], off nt
	global_load_dword v103, v[74:75], off nt
	global_load_dword v104, v[80:81], off nt
	global_load_dword v105, v[78:79], off nt
	global_load_dword v106, v[84:85], off nt
	global_load_dword v107, v[82:83], off nt
	global_load_dword v108, v[88:89], off nt
	global_load_dword v109, v[86:87], off nt
	s_add_i32 s31, s31, 16
	s_add_i32 s21, s21, 16
	s_add_i32 s35, s35, -16
	v_mad_u64_u32 v[4:5], s[38:39], v31, s43, v[10:11]
	s_cmp_lg_u32 s35, 0
	v_mad_u64_u32 v[56:57], s[38:39], v21, s43, v[10:11]
	v_mad_u64_u32 v[58:59], s[38:39], v35, s43, v[10:11]
	v_mad_u64_u32 v[64:65], s[38:39], v33, s43, v[10:11]
	v_mad_u64_u32 v[66:67], s[38:39], v39, s43, v[10:11]
	v_mad_u64_u32 v[68:69], s[38:39], v37, s43, v[10:11]
	v_mad_u64_u32 v[70:71], s[38:39], v43, s43, v[10:11]
	v_mad_u64_u32 v[72:73], s[38:39], v41, s43, v[10:11]
	v_mad_u64_u32 v[74:75], s[38:39], v49, s43, v[10:11]
	v_mad_u64_u32 v[76:77], s[38:39], v47, s43, v[10:11]
	v_mad_u64_u32 v[78:79], s[38:39], v53, s43, v[10:11]
	v_mad_u64_u32 v[80:81], s[38:39], v51, s43, v[10:11]
	v_mad_u64_u32 v[82:83], s[38:39], v91, s43, v[10:11]
	v_mad_u64_u32 v[84:85], s[38:39], v90, s43, v[10:11]
	v_mad_u64_u32 v[86:87], s[38:39], v93, s43, v[10:11]
	v_mad_u64_u32 v[88:89], s[38:39], v92, s43, v[10:11]
	s_lshl_b32 s38, s21, 1
	s_lshl_b32 s39, s31, 1
	v_or_b32_e32 v112, s38, v1
	v_or_b32_e32 v113, s39, v6
	s_add_i32 s40, s38, 4
	s_add_i32 s41, s39, 4
	s_add_i32 s49, s38, 8
	s_add_i32 s50, s39, 8
	s_add_i32 s51, s38, 12
	s_add_i32 s52, s39, 12
	s_add_i32 s53, s38, 16
	s_add_i32 s54, s39, 16
	s_add_i32 s55, s38, 20
	s_add_i32 s56, s39, 20
	s_add_i32 s57, s38, 24
	s_add_i32 s58, s39, 24
	s_add_i32 s38, s38, 28
	s_add_i32 s39, s39, 28
	v_add_u32_e32 v124, s34, v113
	v_or_b32_e32 v114, s40, v1
	v_or_b32_e32 v115, s41, v6
	v_or_b32_e32 v116, s49, v1
	v_or_b32_e32 v117, s50, v6
	v_or_b32_e32 v118, s51, v1
	v_or_b32_e32 v119, s52, v6
	v_or_b32_e32 v120, s53, v1
	v_or_b32_e32 v121, s54, v6
	v_or_b32_e32 v122, s55, v1
	v_or_b32_e32 v123, s56, v6
	v_or_b32_e32 v154, s57, v1
	v_or_b32_e32 v155, s58, v6
	v_or_b32_e32 v156, s38, v1
	v_or_b32_e32 v157, s39, v6
	v_add_u32_e32 v110, s20, v112
	v_ashrrev_i32_e32 v125, 31, v124
	v_add_u32_e32 v126, s20, v114
	v_add_u32_e32 v128, s34, v115
	v_add_u32_e32 v130, s20, v116
	v_add_u32_e32 v132, s34, v117
	v_add_u32_e32 v134, s20, v118
	v_add_u32_e32 v136, s34, v119
	v_add_u32_e32 v138, s20, v120
	v_add_u32_e32 v140, s34, v121
	v_add_u32_e32 v142, s20, v122
	v_add_u32_e32 v144, s34, v123
	v_add_u32_e32 v146, s20, v154
	v_add_u32_e32 v148, s34, v155
	v_add_u32_e32 v150, s20, v156
	v_add_u32_e32 v152, s34, v157
	v_ashrrev_i32_e32 v111, 31, v110
	v_lshlrev_b64 v[124:125], 12, v[124:125]
	v_ashrrev_i32_e32 v129, 31, v128
	v_ashrrev_i32_e32 v127, 31, v126
	v_ashrrev_i32_e32 v133, 31, v132
	v_ashrrev_i32_e32 v131, 31, v130
	v_ashrrev_i32_e32 v137, 31, v136
	v_ashrrev_i32_e32 v135, 31, v134
	v_ashrrev_i32_e32 v141, 31, v140
	v_ashrrev_i32_e32 v139, 31, v138
	v_ashrrev_i32_e32 v145, 31, v144
	v_ashrrev_i32_e32 v143, 31, v142
	v_ashrrev_i32_e32 v149, 31, v148
	v_ashrrev_i32_e32 v147, 31, v146
	v_ashrrev_i32_e32 v153, 31, v152
	v_ashrrev_i32_e32 v151, 31, v150
	v_lshlrev_b64 v[110:111], 12, v[110:111]
	v_lshl_add_u64 v[124:125], v[2:3], 0, v[124:125]
	v_lshlrev_b64 v[126:127], 12, v[126:127]
	v_lshlrev_b64 v[128:129], 12, v[128:129]
	v_lshlrev_b64 v[130:131], 12, v[130:131]
	v_lshlrev_b64 v[132:133], 12, v[132:133]
	v_lshlrev_b64 v[134:135], 12, v[134:135]
	v_lshlrev_b64 v[136:137], 12, v[136:137]
	v_lshlrev_b64 v[138:139], 12, v[138:139]
	v_lshlrev_b64 v[140:141], 12, v[140:141]
	v_lshlrev_b64 v[142:143], 12, v[142:143]
	v_lshlrev_b64 v[144:145], 12, v[144:145]
	v_lshlrev_b64 v[146:147], 12, v[146:147]
	v_lshlrev_b64 v[148:149], 12, v[148:149]
	v_lshlrev_b64 v[150:151], 12, v[150:151]
	v_lshlrev_b64 v[152:153], 12, v[152:153]
	v_lshl_add_u64 v[110:111], v[2:3], 0, v[110:111]
	v_lshl_add_u64 v[128:129], v[2:3], 0, v[128:129]
	v_lshl_add_u64 v[126:127], v[2:3], 0, v[126:127]
	v_lshl_add_u64 v[132:133], v[2:3], 0, v[132:133]
	v_lshl_add_u64 v[130:131], v[2:3], 0, v[130:131]
	v_lshl_add_u64 v[136:137], v[2:3], 0, v[136:137]
	v_lshl_add_u64 v[134:135], v[2:3], 0, v[134:135]
	v_lshl_add_u64 v[140:141], v[2:3], 0, v[140:141]
	v_lshl_add_u64 v[138:139], v[2:3], 0, v[138:139]
	v_lshl_add_u64 v[144:145], v[2:3], 0, v[144:145]
	v_lshl_add_u64 v[142:143], v[2:3], 0, v[142:143]
	v_lshl_add_u64 v[148:149], v[2:3], 0, v[148:149]
	v_lshl_add_u64 v[146:147], v[2:3], 0, v[146:147]
	v_lshl_add_u64 v[152:153], v[2:3], 0, v[152:153]
	v_lshl_add_u64 v[150:151], v[2:3], 0, v[150:151]
	global_load_dword v158, v[124:125], off nt
	global_load_dword v159, v[110:111], off nt
	global_load_dword v160, v[128:129], off nt
	global_load_dword v161, v[126:127], off nt
	global_load_dword v162, v[132:133], off nt
	global_load_dword v163, v[130:131], off nt
	global_load_dword v164, v[136:137], off nt
	global_load_dword v165, v[134:135], off nt
	global_load_dword v166, v[140:141], off nt
	global_load_dword v167, v[138:139], off nt
	global_load_dword v168, v[144:145], off nt
	global_load_dword v169, v[142:143], off nt
	global_load_dword v170, v[148:149], off nt
	global_load_dword v171, v[146:147], off nt
	global_load_dword v172, v[152:153], off nt
	global_load_dword v173, v[150:151], off nt
	s_add_i32 s31, s31, 16
	s_add_i32 s21, s21, 16
	s_add_i32 s35, s35, -16
	v_mad_u64_u32 v[110:111], s[38:39], v113, s43, v[10:11]
	s_cmp_lg_u32 s35, 0
	v_mad_u64_u32 v[124:125], s[38:39], v112, s43, v[10:11]
	v_mad_u64_u32 v[126:127], s[38:39], v115, s43, v[10:11]
	v_mad_u64_u32 v[128:129], s[38:39], v114, s43, v[10:11]
	v_mad_u64_u32 v[130:131], s[38:39], v117, s43, v[10:11]
	v_mad_u64_u32 v[132:133], s[38:39], v116, s43, v[10:11]
	v_mad_u64_u32 v[134:135], s[38:39], v119, s43, v[10:11]
	v_mad_u64_u32 v[136:137], s[38:39], v118, s43, v[10:11]
	v_mad_u64_u32 v[138:139], s[38:39], v121, s43, v[10:11]
	v_mad_u64_u32 v[140:141], s[38:39], v120, s43, v[10:11]
	v_mad_u64_u32 v[142:143], s[38:39], v123, s43, v[10:11]
	v_mad_u64_u32 v[144:145], s[38:39], v122, s43, v[10:11]
	v_mad_u64_u32 v[146:147], s[38:39], v155, s43, v[10:11]
	v_mad_u64_u32 v[148:149], s[38:39], v154, s43, v[10:11]
	v_mad_u64_u32 v[150:151], s[38:39], v157, s43, v[10:11]
	v_mad_u64_u32 v[152:153], s[38:39], v156, s43, v[10:11]
	s_waitcnt vmcnt(31)
	ds_write_b32 v4, v94
	s_waitcnt vmcnt(30)
	ds_write_b32 v56, v95
	s_waitcnt vmcnt(29)
	ds_write_b32 v58, v96
	s_waitcnt vmcnt(28)
	ds_write_b32 v64, v97
	s_waitcnt vmcnt(27)
	ds_write_b32 v66, v98
	s_waitcnt vmcnt(26)
	ds_write_b32 v68, v99
	s_waitcnt vmcnt(25)
	ds_write_b32 v70, v100
	s_waitcnt vmcnt(24)
	ds_write_b32 v72, v101
	s_waitcnt vmcnt(23)
	ds_write_b32 v74, v102
	s_waitcnt vmcnt(22)
	ds_write_b32 v76, v103
	s_waitcnt vmcnt(21)
	ds_write_b32 v78, v104
	s_waitcnt vmcnt(20)
	ds_write_b32 v80, v105
	s_waitcnt vmcnt(19)
	ds_write_b32 v82, v106
	s_waitcnt vmcnt(18)
	ds_write_b32 v84, v107
	s_waitcnt vmcnt(17)
	ds_write_b32 v86, v108
	s_waitcnt vmcnt(16)
	ds_write_b32 v88, v109
	s_waitcnt vmcnt(15)
	ds_write_b32 v110, v158
	s_waitcnt vmcnt(14)
	ds_write_b32 v124, v159
	s_waitcnt vmcnt(13)
	ds_write_b32 v126, v160
	s_waitcnt vmcnt(12)
	ds_write_b32 v128, v161
	s_waitcnt vmcnt(11)
	ds_write_b32 v130, v162
	s_waitcnt vmcnt(10)
	ds_write_b32 v132, v163
	s_waitcnt vmcnt(9)
	ds_write_b32 v134, v164
	s_waitcnt vmcnt(8)
	ds_write_b32 v136, v165
	s_waitcnt vmcnt(7)
	ds_write_b32 v138, v166
	s_waitcnt vmcnt(6)
	ds_write_b32 v140, v167
	s_waitcnt vmcnt(5)
	ds_write_b32 v142, v168
	s_waitcnt vmcnt(4)
	ds_write_b32 v144, v169
	s_waitcnt vmcnt(3)
	ds_write_b32 v146, v170
	s_waitcnt vmcnt(2)
	ds_write_b32 v148, v171
	s_waitcnt vmcnt(1)
	ds_write_b32 v150, v172
	s_waitcnt vmcnt(0)
	ds_write_b32 v152, v173

.LBB0_155:
	s_lshl_b32 s36, s21, 1
	s_lshl_b32 s37, s27, 1
	v_or_b32_e32 v21, s36, v1
	v_or_b32_e32 v31, s37, v6
	s_add_i32 s38, s36, 4
	s_add_i32 s39, s37, 4
	s_add_i32 s40, s36, 8
	s_add_i32 s41, s37, 8
	s_add_i32 s49, s36, 12
	s_add_i32 s50, s37, 12
	s_add_i32 s51, s36, 16
	s_add_i32 s52, s37, 16
	s_add_i32 s53, s36, 20
	s_add_i32 s54, s37, 20
	s_add_i32 s55, s36, 24
	s_add_i32 s56, s37, 24
	s_add_i32 s36, s36, 28
	s_add_i32 s37, s37, 28
	v_add_u32_e32 v56, s30, v31
	v_or_b32_e32 v33, s38, v1
	v_or_b32_e32 v35, s39, v6
	v_or_b32_e32 v37, s40, v1
	v_or_b32_e32 v39, s41, v6
	v_or_b32_e32 v41, s49, v1
	v_or_b32_e32 v43, s50, v6
	v_or_b32_e32 v47, s51, v1
	v_or_b32_e32 v49, s52, v6
	v_or_b32_e32 v51, s53, v1
	v_or_b32_e32 v53, s54, v6
	v_or_b32_e32 v90, s55, v1
	v_or_b32_e32 v91, s56, v6
	v_or_b32_e32 v92, s36, v1
	v_or_b32_e32 v93, s37, v6
	v_add_u32_e32 v4, s20, v21
	v_ashrrev_i32_e32 v57, 31, v56
	v_add_u32_e32 v58, s20, v33
	v_add_u32_e32 v64, s30, v35
	v_add_u32_e32 v66, s20, v37
	v_add_u32_e32 v68, s30, v39
	v_add_u32_e32 v70, s20, v41
	v_add_u32_e32 v72, s30, v43
	v_add_u32_e32 v74, s20, v47
	v_add_u32_e32 v76, s30, v49
	v_add_u32_e32 v78, s20, v51
	v_add_u32_e32 v80, s30, v53
	v_add_u32_e32 v82, s20, v90
	v_add_u32_e32 v84, s30, v91
	v_add_u32_e32 v86, s20, v92
	v_add_u32_e32 v88, s30, v93
	v_ashrrev_i32_e32 v5, 31, v4
	v_lshlrev_b64 v[56:57], 12, v[56:57]
	v_ashrrev_i32_e32 v65, 31, v64
	v_ashrrev_i32_e32 v59, 31, v58
	v_ashrrev_i32_e32 v69, 31, v68
	v_ashrrev_i32_e32 v67, 31, v66
	v_ashrrev_i32_e32 v73, 31, v72
	v_ashrrev_i32_e32 v71, 31, v70
	v_ashrrev_i32_e32 v77, 31, v76
	v_ashrrev_i32_e32 v75, 31, v74
	v_ashrrev_i32_e32 v81, 31, v80
	v_ashrrev_i32_e32 v79, 31, v78
	v_ashrrev_i32_e32 v85, 31, v84
	v_ashrrev_i32_e32 v83, 31, v82
	v_ashrrev_i32_e32 v89, 31, v88
	v_ashrrev_i32_e32 v87, 31, v86
	v_lshlrev_b64 v[4:5], 12, v[4:5]
	v_lshl_add_u64 v[56:57], v[2:3], 0, v[56:57]
	v_lshlrev_b64 v[58:59], 12, v[58:59]
	v_lshlrev_b64 v[64:65], 12, v[64:65]
	v_lshlrev_b64 v[66:67], 12, v[66:67]
	v_lshlrev_b64 v[68:69], 12, v[68:69]
	v_lshlrev_b64 v[70:71], 12, v[70:71]
	v_lshlrev_b64 v[72:73], 12, v[72:73]
	v_lshlrev_b64 v[74:75], 12, v[74:75]
	v_lshlrev_b64 v[76:77], 12, v[76:77]
	v_lshlrev_b64 v[78:79], 12, v[78:79]
	v_lshlrev_b64 v[80:81], 12, v[80:81]
	v_lshlrev_b64 v[82:83], 12, v[82:83]
	v_lshlrev_b64 v[84:85], 12, v[84:85]
	v_lshlrev_b64 v[86:87], 12, v[86:87]
	v_lshlrev_b64 v[88:89], 12, v[88:89]
	v_lshl_add_u64 v[4:5], v[2:3], 0, v[4:5]
	v_lshl_add_u64 v[64:65], v[2:3], 0, v[64:65]
	v_lshl_add_u64 v[58:59], v[2:3], 0, v[58:59]
	v_lshl_add_u64 v[68:69], v[2:3], 0, v[68:69]
	v_lshl_add_u64 v[66:67], v[2:3], 0, v[66:67]
	v_lshl_add_u64 v[72:73], v[2:3], 0, v[72:73]
	v_lshl_add_u64 v[70:71], v[2:3], 0, v[70:71]
	v_lshl_add_u64 v[76:77], v[2:3], 0, v[76:77]
	v_lshl_add_u64 v[74:75], v[2:3], 0, v[74:75]
	v_lshl_add_u64 v[80:81], v[2:3], 0, v[80:81]
	v_lshl_add_u64 v[78:79], v[2:3], 0, v[78:79]
	v_lshl_add_u64 v[84:85], v[2:3], 0, v[84:85]
	v_lshl_add_u64 v[82:83], v[2:3], 0, v[82:83]
	v_lshl_add_u64 v[88:89], v[2:3], 0, v[88:89]
	v_lshl_add_u64 v[86:87], v[2:3], 0, v[86:87]
	global_load_dword v94, v[56:57], off nt
	global_load_dword v95, v[4:5], off nt
	global_load_dword v96, v[64:65], off nt
	global_load_dword v97, v[58:59], off nt
	global_load_dword v98, v[68:69], off nt
	global_load_dword v99, v[66:67], off nt
	global_load_dword v100, v[72:73], off nt
	global_load_dword v101, v[70:71], off nt
	global_load_dword v102, v[76:77], off nt
	global_load_dword v103, v[74:75], off nt
	global_load_dword v104, v[80:81], off nt
	global_load_dword v105, v[78:79], off nt
	global_load_dword v106, v[84:85], off nt
	global_load_dword v107, v[82:83], off nt
	global_load_dword v108, v[88:89], off nt
	global_load_dword v109, v[86:87], off nt
	s_add_i32 s27, s27, 16
	s_add_i32 s21, s21, 16
	s_add_i32 s31, s31, -16
	v_mad_u64_u32 v[4:5], s[36:37], v31, s43, v[10:11]
	s_cmp_lg_u32 s31, 0
	v_mad_u64_u32 v[56:57], s[36:37], v21, s43, v[10:11]
	v_mad_u64_u32 v[58:59], s[36:37], v35, s43, v[10:11]
	v_mad_u64_u32 v[64:65], s[36:37], v33, s43, v[10:11]
	v_mad_u64_u32 v[66:67], s[36:37], v39, s43, v[10:11]
	v_mad_u64_u32 v[68:69], s[36:37], v37, s43, v[10:11]
	v_mad_u64_u32 v[70:71], s[36:37], v43, s43, v[10:11]
	v_mad_u64_u32 v[72:73], s[36:37], v41, s43, v[10:11]
	v_mad_u64_u32 v[74:75], s[36:37], v49, s43, v[10:11]
	v_mad_u64_u32 v[76:77], s[36:37], v47, s43, v[10:11]
	v_mad_u64_u32 v[78:79], s[36:37], v53, s43, v[10:11]
	v_mad_u64_u32 v[80:81], s[36:37], v51, s43, v[10:11]
	v_mad_u64_u32 v[82:83], s[36:37], v91, s43, v[10:11]
	v_mad_u64_u32 v[84:85], s[36:37], v90, s43, v[10:11]
	v_mad_u64_u32 v[86:87], s[36:37], v93, s43, v[10:11]
	v_mad_u64_u32 v[88:89], s[36:37], v92, s43, v[10:11]
	s_lshl_b32 s36, s21, 1
	s_lshl_b32 s37, s27, 1
	v_or_b32_e32 v112, s36, v1
	v_or_b32_e32 v113, s37, v6
	s_add_i32 s38, s36, 4
	s_add_i32 s39, s37, 4
	s_add_i32 s40, s36, 8
	s_add_i32 s41, s37, 8
	s_add_i32 s49, s36, 12
	s_add_i32 s50, s37, 12
	s_add_i32 s51, s36, 16
	s_add_i32 s52, s37, 16
	s_add_i32 s53, s36, 20
	s_add_i32 s54, s37, 20
	s_add_i32 s55, s36, 24
	s_add_i32 s56, s37, 24
	s_add_i32 s36, s36, 28
	s_add_i32 s37, s37, 28
	v_add_u32_e32 v124, s30, v113
	v_or_b32_e32 v114, s38, v1
	v_or_b32_e32 v115, s39, v6
	v_or_b32_e32 v116, s40, v1
	v_or_b32_e32 v117, s41, v6
	v_or_b32_e32 v118, s49, v1
	v_or_b32_e32 v119, s50, v6
	v_or_b32_e32 v120, s51, v1
	v_or_b32_e32 v121, s52, v6
	v_or_b32_e32 v122, s53, v1
	v_or_b32_e32 v123, s54, v6
	v_or_b32_e32 v154, s55, v1
	v_or_b32_e32 v155, s56, v6
	v_or_b32_e32 v156, s36, v1
	v_or_b32_e32 v157, s37, v6
	v_add_u32_e32 v110, s20, v112
	v_ashrrev_i32_e32 v125, 31, v124
	v_add_u32_e32 v126, s20, v114
	v_add_u32_e32 v128, s30, v115
	v_add_u32_e32 v130, s20, v116
	v_add_u32_e32 v132, s30, v117
	v_add_u32_e32 v134, s20, v118
	v_add_u32_e32 v136, s30, v119
	v_add_u32_e32 v138, s20, v120
	v_add_u32_e32 v140, s30, v121
	v_add_u32_e32 v142, s20, v122
	v_add_u32_e32 v144, s30, v123
	v_add_u32_e32 v146, s20, v154
	v_add_u32_e32 v148, s30, v155
	v_add_u32_e32 v150, s20, v156
	v_add_u32_e32 v152, s30, v157
	v_ashrrev_i32_e32 v111, 31, v110
	v_lshlrev_b64 v[124:125], 12, v[124:125]
	v_ashrrev_i32_e32 v129, 31, v128
	v_ashrrev_i32_e32 v127, 31, v126
	v_ashrrev_i32_e32 v133, 31, v132
	v_ashrrev_i32_e32 v131, 31, v130
	v_ashrrev_i32_e32 v137, 31, v136
	v_ashrrev_i32_e32 v135, 31, v134
	v_ashrrev_i32_e32 v141, 31, v140
	v_ashrrev_i32_e32 v139, 31, v138
	v_ashrrev_i32_e32 v145, 31, v144
	v_ashrrev_i32_e32 v143, 31, v142
	v_ashrrev_i32_e32 v149, 31, v148
	v_ashrrev_i32_e32 v147, 31, v146
	v_ashrrev_i32_e32 v153, 31, v152
	v_ashrrev_i32_e32 v151, 31, v150
	v_lshlrev_b64 v[110:111], 12, v[110:111]
	v_lshl_add_u64 v[124:125], v[2:3], 0, v[124:125]
	v_lshlrev_b64 v[126:127], 12, v[126:127]
	v_lshlrev_b64 v[128:129], 12, v[128:129]
	v_lshlrev_b64 v[130:131], 12, v[130:131]
	v_lshlrev_b64 v[132:133], 12, v[132:133]
	v_lshlrev_b64 v[134:135], 12, v[134:135]
	v_lshlrev_b64 v[136:137], 12, v[136:137]
	v_lshlrev_b64 v[138:139], 12, v[138:139]
	v_lshlrev_b64 v[140:141], 12, v[140:141]
	v_lshlrev_b64 v[142:143], 12, v[142:143]
	v_lshlrev_b64 v[144:145], 12, v[144:145]
	v_lshlrev_b64 v[146:147], 12, v[146:147]
	v_lshlrev_b64 v[148:149], 12, v[148:149]
	v_lshlrev_b64 v[150:151], 12, v[150:151]
	v_lshlrev_b64 v[152:153], 12, v[152:153]
	v_lshl_add_u64 v[110:111], v[2:3], 0, v[110:111]
	v_lshl_add_u64 v[128:129], v[2:3], 0, v[128:129]
	v_lshl_add_u64 v[126:127], v[2:3], 0, v[126:127]
	v_lshl_add_u64 v[132:133], v[2:3], 0, v[132:133]
	v_lshl_add_u64 v[130:131], v[2:3], 0, v[130:131]
	v_lshl_add_u64 v[136:137], v[2:3], 0, v[136:137]
	v_lshl_add_u64 v[134:135], v[2:3], 0, v[134:135]
	v_lshl_add_u64 v[140:141], v[2:3], 0, v[140:141]
	v_lshl_add_u64 v[138:139], v[2:3], 0, v[138:139]
	v_lshl_add_u64 v[144:145], v[2:3], 0, v[144:145]
	v_lshl_add_u64 v[142:143], v[2:3], 0, v[142:143]
	v_lshl_add_u64 v[148:149], v[2:3], 0, v[148:149]
	v_lshl_add_u64 v[146:147], v[2:3], 0, v[146:147]
	v_lshl_add_u64 v[152:153], v[2:3], 0, v[152:153]
	v_lshl_add_u64 v[150:151], v[2:3], 0, v[150:151]
	global_load_dword v158, v[124:125], off nt
	global_load_dword v159, v[110:111], off nt
	global_load_dword v160, v[128:129], off nt
	global_load_dword v161, v[126:127], off nt
	global_load_dword v162, v[132:133], off nt
	global_load_dword v163, v[130:131], off nt
	global_load_dword v164, v[136:137], off nt
	global_load_dword v165, v[134:135], off nt
	global_load_dword v166, v[140:141], off nt
	global_load_dword v167, v[138:139], off nt
	global_load_dword v168, v[144:145], off nt
	global_load_dword v169, v[142:143], off nt
	global_load_dword v170, v[148:149], off nt
	global_load_dword v171, v[146:147], off nt
	global_load_dword v172, v[152:153], off nt
	global_load_dword v173, v[150:151], off nt
	s_add_i32 s27, s27, 16
	s_add_i32 s21, s21, 16
	s_add_i32 s31, s31, -16
	v_mad_u64_u32 v[110:111], s[36:37], v113, s43, v[10:11]
	s_cmp_lg_u32 s31, 0
	v_mad_u64_u32 v[124:125], s[36:37], v112, s43, v[10:11]
	v_mad_u64_u32 v[126:127], s[36:37], v115, s43, v[10:11]
	v_mad_u64_u32 v[128:129], s[36:37], v114, s43, v[10:11]
	v_mad_u64_u32 v[130:131], s[36:37], v117, s43, v[10:11]
	v_mad_u64_u32 v[132:133], s[36:37], v116, s43, v[10:11]
	v_mad_u64_u32 v[134:135], s[36:37], v119, s43, v[10:11]
	v_mad_u64_u32 v[136:137], s[36:37], v118, s43, v[10:11]
	v_mad_u64_u32 v[138:139], s[36:37], v121, s43, v[10:11]
	v_mad_u64_u32 v[140:141], s[36:37], v120, s43, v[10:11]
	v_mad_u64_u32 v[142:143], s[36:37], v123, s43, v[10:11]
	v_mad_u64_u32 v[144:145], s[36:37], v122, s43, v[10:11]
	v_mad_u64_u32 v[146:147], s[36:37], v155, s43, v[10:11]
	v_mad_u64_u32 v[148:149], s[36:37], v154, s43, v[10:11]
	v_mad_u64_u32 v[150:151], s[36:37], v157, s43, v[10:11]
	v_mad_u64_u32 v[152:153], s[36:37], v156, s43, v[10:11]
	s_waitcnt vmcnt(31)
	ds_write_b32 v4, v94
	s_waitcnt vmcnt(30)
	ds_write_b32 v56, v95
	s_waitcnt vmcnt(29)
	ds_write_b32 v58, v96
	s_waitcnt vmcnt(28)
	ds_write_b32 v64, v97
	s_waitcnt vmcnt(27)
	ds_write_b32 v66, v98
	s_waitcnt vmcnt(26)
	ds_write_b32 v68, v99
	s_waitcnt vmcnt(25)
	ds_write_b32 v70, v100
	s_waitcnt vmcnt(24)
	ds_write_b32 v72, v101
	s_waitcnt vmcnt(23)
	ds_write_b32 v74, v102
	s_waitcnt vmcnt(22)
	ds_write_b32 v76, v103
	s_waitcnt vmcnt(21)
	ds_write_b32 v78, v104
	s_waitcnt vmcnt(20)
	ds_write_b32 v80, v105
	s_waitcnt vmcnt(19)
	ds_write_b32 v82, v106
	s_waitcnt vmcnt(18)
	ds_write_b32 v84, v107
	s_waitcnt vmcnt(17)
	ds_write_b32 v86, v108
	s_waitcnt vmcnt(16)
	ds_write_b32 v88, v109
	s_waitcnt vmcnt(15)
	ds_write_b32 v110, v158
	s_waitcnt vmcnt(14)
	ds_write_b32 v124, v159
	s_waitcnt vmcnt(13)
	ds_write_b32 v126, v160
	s_waitcnt vmcnt(12)
	ds_write_b32 v128, v161
	s_waitcnt vmcnt(11)
	ds_write_b32 v130, v162
	s_waitcnt vmcnt(10)
	ds_write_b32 v132, v163
	s_waitcnt vmcnt(9)
	ds_write_b32 v134, v164
	s_waitcnt vmcnt(8)
	ds_write_b32 v136, v165
	s_waitcnt vmcnt(7)
	ds_write_b32 v138, v166
	s_waitcnt vmcnt(6)
	ds_write_b32 v140, v167
	s_waitcnt vmcnt(5)
	ds_write_b32 v142, v168
	s_waitcnt vmcnt(4)
	ds_write_b32 v144, v169
	s_waitcnt vmcnt(3)
	ds_write_b32 v146, v170
	s_waitcnt vmcnt(2)
	ds_write_b32 v148, v171
	s_waitcnt vmcnt(1)
	ds_write_b32 v150, v172
	s_waitcnt vmcnt(0)
	ds_write_b32 v152, v173

.LBB0_169:
	s_lshl_b32 s31, s21, 1
	s_lshl_b32 s36, s23, 1
	v_or_b32_e32 v21, s31, v1
	v_or_b32_e32 v31, s36, v6
	s_add_i32 s37, s31, 4
	s_add_i32 s38, s36, 4
	s_add_i32 s39, s31, 8
	s_add_i32 s40, s36, 8
	s_add_i32 s41, s31, 12
	s_add_i32 s47, s36, 12
	s_add_i32 s48, s31, 16
	s_add_i32 s49, s36, 16
	s_add_i32 s50, s31, 20
	s_add_i32 s51, s36, 20
	s_add_i32 s52, s31, 24
	s_add_i32 s53, s36, 24
	s_add_i32 s31, s31, 28
	s_add_i32 s36, s36, 28
	v_add_u32_e32 v56, s30, v31
	v_or_b32_e32 v33, s37, v1
	v_or_b32_e32 v35, s38, v6
	v_or_b32_e32 v37, s39, v1
	v_or_b32_e32 v39, s40, v6
	v_or_b32_e32 v41, s41, v1
	v_or_b32_e32 v43, s47, v6
	v_or_b32_e32 v47, s48, v1
	v_or_b32_e32 v49, s49, v6
	v_or_b32_e32 v51, s50, v1
	v_or_b32_e32 v53, s51, v6
	v_or_b32_e32 v90, s52, v1
	v_or_b32_e32 v91, s53, v6
	v_or_b32_e32 v92, s31, v1
	v_or_b32_e32 v93, s36, v6
	v_add_u32_e32 v4, s20, v21
	v_ashrrev_i32_e32 v57, 31, v56
	v_add_u32_e32 v58, s20, v33
	v_add_u32_e32 v64, s30, v35
	v_add_u32_e32 v66, s20, v37
	v_add_u32_e32 v68, s30, v39
	v_add_u32_e32 v70, s20, v41
	v_add_u32_e32 v72, s30, v43
	v_add_u32_e32 v74, s20, v47
	v_add_u32_e32 v76, s30, v49
	v_add_u32_e32 v78, s20, v51
	v_add_u32_e32 v80, s30, v53
	v_add_u32_e32 v82, s20, v90
	v_add_u32_e32 v84, s30, v91
	v_add_u32_e32 v86, s20, v92
	v_add_u32_e32 v88, s30, v93
	v_ashrrev_i32_e32 v5, 31, v4
	v_lshlrev_b64 v[56:57], 12, v[56:57]
	v_ashrrev_i32_e32 v65, 31, v64
	v_ashrrev_i32_e32 v59, 31, v58
	v_ashrrev_i32_e32 v69, 31, v68
	v_ashrrev_i32_e32 v67, 31, v66
	v_ashrrev_i32_e32 v73, 31, v72
	v_ashrrev_i32_e32 v71, 31, v70
	v_ashrrev_i32_e32 v77, 31, v76
	v_ashrrev_i32_e32 v75, 31, v74
	v_ashrrev_i32_e32 v81, 31, v80
	v_ashrrev_i32_e32 v79, 31, v78
	v_ashrrev_i32_e32 v85, 31, v84
	v_ashrrev_i32_e32 v83, 31, v82
	v_ashrrev_i32_e32 v89, 31, v88
	v_ashrrev_i32_e32 v87, 31, v86
	v_lshlrev_b64 v[4:5], 12, v[4:5]
	v_lshl_add_u64 v[56:57], v[2:3], 0, v[56:57]
	v_lshlrev_b64 v[58:59], 12, v[58:59]
	v_lshlrev_b64 v[64:65], 12, v[64:65]
	v_lshlrev_b64 v[66:67], 12, v[66:67]
	v_lshlrev_b64 v[68:69], 12, v[68:69]
	v_lshlrev_b64 v[70:71], 12, v[70:71]
	v_lshlrev_b64 v[72:73], 12, v[72:73]
	v_lshlrev_b64 v[74:75], 12, v[74:75]
	v_lshlrev_b64 v[76:77], 12, v[76:77]
	v_lshlrev_b64 v[78:79], 12, v[78:79]
	v_lshlrev_b64 v[80:81], 12, v[80:81]
	v_lshlrev_b64 v[82:83], 12, v[82:83]
	v_lshlrev_b64 v[84:85], 12, v[84:85]
	v_lshlrev_b64 v[86:87], 12, v[86:87]
	v_lshlrev_b64 v[88:89], 12, v[88:89]
	v_lshl_add_u64 v[4:5], v[2:3], 0, v[4:5]
	v_lshl_add_u64 v[64:65], v[2:3], 0, v[64:65]
	v_lshl_add_u64 v[58:59], v[2:3], 0, v[58:59]
	v_lshl_add_u64 v[68:69], v[2:3], 0, v[68:69]
	v_lshl_add_u64 v[66:67], v[2:3], 0, v[66:67]
	v_lshl_add_u64 v[72:73], v[2:3], 0, v[72:73]
	v_lshl_add_u64 v[70:71], v[2:3], 0, v[70:71]
	v_lshl_add_u64 v[76:77], v[2:3], 0, v[76:77]
	v_lshl_add_u64 v[74:75], v[2:3], 0, v[74:75]
	v_lshl_add_u64 v[80:81], v[2:3], 0, v[80:81]
	v_lshl_add_u64 v[78:79], v[2:3], 0, v[78:79]
	v_lshl_add_u64 v[84:85], v[2:3], 0, v[84:85]
	v_lshl_add_u64 v[82:83], v[2:3], 0, v[82:83]
	v_lshl_add_u64 v[88:89], v[2:3], 0, v[88:89]
	v_lshl_add_u64 v[86:87], v[2:3], 0, v[86:87]
	global_load_dword v94, v[56:57], off nt
	global_load_dword v95, v[4:5], off nt
	global_load_dword v96, v[64:65], off nt
	global_load_dword v97, v[58:59], off nt
	global_load_dword v98, v[68:69], off nt
	global_load_dword v99, v[66:67], off nt
	global_load_dword v100, v[72:73], off nt
	global_load_dword v101, v[70:71], off nt
	global_load_dword v102, v[76:77], off nt
	global_load_dword v103, v[74:75], off nt
	global_load_dword v104, v[80:81], off nt
	global_load_dword v105, v[78:79], off nt
	global_load_dword v106, v[84:85], off nt
	global_load_dword v107, v[82:83], off nt
	global_load_dword v108, v[88:89], off nt
	global_load_dword v109, v[86:87], off nt
	s_add_i32 s23, s23, 16
	s_add_i32 s21, s21, 16
	s_add_i32 s27, s27, -16
	v_mad_u64_u32 v[4:5], s[36:37], v31, s43, v[10:11]
	s_cmp_lg_u32 s27, 0
	v_mad_u64_u32 v[56:57], s[36:37], v21, s43, v[10:11]
	v_mad_u64_u32 v[58:59], s[36:37], v35, s43, v[10:11]
	v_mad_u64_u32 v[64:65], s[36:37], v33, s43, v[10:11]
	v_mad_u64_u32 v[66:67], s[36:37], v39, s43, v[10:11]
	v_mad_u64_u32 v[68:69], s[36:37], v37, s43, v[10:11]
	v_mad_u64_u32 v[70:71], s[36:37], v43, s43, v[10:11]
	v_mad_u64_u32 v[72:73], s[36:37], v41, s43, v[10:11]
	v_mad_u64_u32 v[74:75], s[36:37], v49, s43, v[10:11]
	v_mad_u64_u32 v[76:77], s[36:37], v47, s43, v[10:11]
	v_mad_u64_u32 v[78:79], s[36:37], v53, s43, v[10:11]
	v_mad_u64_u32 v[80:81], s[36:37], v51, s43, v[10:11]
	v_mad_u64_u32 v[82:83], s[36:37], v91, s43, v[10:11]
	v_mad_u64_u32 v[84:85], s[36:37], v90, s43, v[10:11]
	v_mad_u64_u32 v[86:87], s[36:37], v93, s43, v[10:11]
	v_mad_u64_u32 v[88:89], s[36:37], v92, s43, v[10:11]
	s_lshl_b32 s31, s21, 1
	s_lshl_b32 s36, s23, 1
	v_or_b32_e32 v112, s31, v1
	v_or_b32_e32 v113, s36, v6
	s_add_i32 s37, s31, 4
	s_add_i32 s38, s36, 4
	s_add_i32 s39, s31, 8
	s_add_i32 s40, s36, 8
	s_add_i32 s41, s31, 12
	s_add_i32 s47, s36, 12
	s_add_i32 s48, s31, 16
	s_add_i32 s49, s36, 16
	s_add_i32 s50, s31, 20
	s_add_i32 s51, s36, 20
	s_add_i32 s52, s31, 24
	s_add_i32 s53, s36, 24
	s_add_i32 s31, s31, 28
	s_add_i32 s36, s36, 28
	v_add_u32_e32 v124, s30, v113
	v_or_b32_e32 v114, s37, v1
	v_or_b32_e32 v115, s38, v6
	v_or_b32_e32 v116, s39, v1
	v_or_b32_e32 v117, s40, v6
	v_or_b32_e32 v118, s41, v1
	v_or_b32_e32 v119, s47, v6
	v_or_b32_e32 v120, s48, v1
	v_or_b32_e32 v121, s49, v6
	v_or_b32_e32 v122, s50, v1
	v_or_b32_e32 v123, s51, v6
	v_or_b32_e32 v154, s52, v1
	v_or_b32_e32 v155, s53, v6
	v_or_b32_e32 v156, s31, v1
	v_or_b32_e32 v157, s36, v6
	v_add_u32_e32 v110, s20, v112
	v_ashrrev_i32_e32 v125, 31, v124
	v_add_u32_e32 v126, s20, v114
	v_add_u32_e32 v128, s30, v115
	v_add_u32_e32 v130, s20, v116
	v_add_u32_e32 v132, s30, v117
	v_add_u32_e32 v134, s20, v118
	v_add_u32_e32 v136, s30, v119
	v_add_u32_e32 v138, s20, v120
	v_add_u32_e32 v140, s30, v121
	v_add_u32_e32 v142, s20, v122
	v_add_u32_e32 v144, s30, v123
	v_add_u32_e32 v146, s20, v154
	v_add_u32_e32 v148, s30, v155
	v_add_u32_e32 v150, s20, v156
	v_add_u32_e32 v152, s30, v157
	v_ashrrev_i32_e32 v111, 31, v110
	v_lshlrev_b64 v[124:125], 12, v[124:125]
	v_ashrrev_i32_e32 v129, 31, v128
	v_ashrrev_i32_e32 v127, 31, v126
	v_ashrrev_i32_e32 v133, 31, v132
	v_ashrrev_i32_e32 v131, 31, v130
	v_ashrrev_i32_e32 v137, 31, v136
	v_ashrrev_i32_e32 v135, 31, v134
	v_ashrrev_i32_e32 v141, 31, v140
	v_ashrrev_i32_e32 v139, 31, v138
	v_ashrrev_i32_e32 v145, 31, v144
	v_ashrrev_i32_e32 v143, 31, v142
	v_ashrrev_i32_e32 v149, 31, v148
	v_ashrrev_i32_e32 v147, 31, v146
	v_ashrrev_i32_e32 v153, 31, v152
	v_ashrrev_i32_e32 v151, 31, v150
	v_lshlrev_b64 v[110:111], 12, v[110:111]
	v_lshl_add_u64 v[124:125], v[2:3], 0, v[124:125]
	v_lshlrev_b64 v[126:127], 12, v[126:127]
	v_lshlrev_b64 v[128:129], 12, v[128:129]
	v_lshlrev_b64 v[130:131], 12, v[130:131]
	v_lshlrev_b64 v[132:133], 12, v[132:133]
	v_lshlrev_b64 v[134:135], 12, v[134:135]
	v_lshlrev_b64 v[136:137], 12, v[136:137]
	v_lshlrev_b64 v[138:139], 12, v[138:139]
	v_lshlrev_b64 v[140:141], 12, v[140:141]
	v_lshlrev_b64 v[142:143], 12, v[142:143]
	v_lshlrev_b64 v[144:145], 12, v[144:145]
	v_lshlrev_b64 v[146:147], 12, v[146:147]
	v_lshlrev_b64 v[148:149], 12, v[148:149]
	v_lshlrev_b64 v[150:151], 12, v[150:151]
	v_lshlrev_b64 v[152:153], 12, v[152:153]
	v_lshl_add_u64 v[110:111], v[2:3], 0, v[110:111]
	v_lshl_add_u64 v[128:129], v[2:3], 0, v[128:129]
	v_lshl_add_u64 v[126:127], v[2:3], 0, v[126:127]
	v_lshl_add_u64 v[132:133], v[2:3], 0, v[132:133]
	v_lshl_add_u64 v[130:131], v[2:3], 0, v[130:131]
	v_lshl_add_u64 v[136:137], v[2:3], 0, v[136:137]
	v_lshl_add_u64 v[134:135], v[2:3], 0, v[134:135]
	v_lshl_add_u64 v[140:141], v[2:3], 0, v[140:141]
	v_lshl_add_u64 v[138:139], v[2:3], 0, v[138:139]
	v_lshl_add_u64 v[144:145], v[2:3], 0, v[144:145]
	v_lshl_add_u64 v[142:143], v[2:3], 0, v[142:143]
	v_lshl_add_u64 v[148:149], v[2:3], 0, v[148:149]
	v_lshl_add_u64 v[146:147], v[2:3], 0, v[146:147]
	v_lshl_add_u64 v[152:153], v[2:3], 0, v[152:153]
	v_lshl_add_u64 v[150:151], v[2:3], 0, v[150:151]
	global_load_dword v158, v[124:125], off nt
	global_load_dword v159, v[110:111], off nt
	global_load_dword v160, v[128:129], off nt
	global_load_dword v161, v[126:127], off nt
	global_load_dword v162, v[132:133], off nt
	global_load_dword v163, v[130:131], off nt
	global_load_dword v164, v[136:137], off nt
	global_load_dword v165, v[134:135], off nt
	global_load_dword v166, v[140:141], off nt
	global_load_dword v167, v[138:139], off nt
	global_load_dword v168, v[144:145], off nt
	global_load_dword v169, v[142:143], off nt
	global_load_dword v170, v[148:149], off nt
	global_load_dword v171, v[146:147], off nt
	global_load_dword v172, v[152:153], off nt
	global_load_dword v173, v[150:151], off nt
	s_add_i32 s23, s23, 16
	s_add_i32 s21, s21, 16
	s_add_i32 s27, s27, -16
	v_mad_u64_u32 v[110:111], s[36:37], v113, s43, v[10:11]
	s_cmp_lg_u32 s27, 0
	v_mad_u64_u32 v[124:125], s[36:37], v112, s43, v[10:11]
	v_mad_u64_u32 v[126:127], s[36:37], v115, s43, v[10:11]
	v_mad_u64_u32 v[128:129], s[36:37], v114, s43, v[10:11]
	v_mad_u64_u32 v[130:131], s[36:37], v117, s43, v[10:11]
	v_mad_u64_u32 v[132:133], s[36:37], v116, s43, v[10:11]
	v_mad_u64_u32 v[134:135], s[36:37], v119, s43, v[10:11]
	v_mad_u64_u32 v[136:137], s[36:37], v118, s43, v[10:11]
	v_mad_u64_u32 v[138:139], s[36:37], v121, s43, v[10:11]
	v_mad_u64_u32 v[140:141], s[36:37], v120, s43, v[10:11]
	v_mad_u64_u32 v[142:143], s[36:37], v123, s43, v[10:11]
	v_mad_u64_u32 v[144:145], s[36:37], v122, s43, v[10:11]
	v_mad_u64_u32 v[146:147], s[36:37], v155, s43, v[10:11]
	v_mad_u64_u32 v[148:149], s[36:37], v154, s43, v[10:11]
	v_mad_u64_u32 v[150:151], s[36:37], v157, s43, v[10:11]
	v_mad_u64_u32 v[152:153], s[36:37], v156, s43, v[10:11]
	s_waitcnt vmcnt(31)
	ds_write_b32 v4, v94
	s_waitcnt vmcnt(30)
	ds_write_b32 v56, v95
	s_waitcnt vmcnt(29)
	ds_write_b32 v58, v96
	s_waitcnt vmcnt(28)
	ds_write_b32 v64, v97
	s_waitcnt vmcnt(27)
	ds_write_b32 v66, v98
	s_waitcnt vmcnt(26)
	ds_write_b32 v68, v99
	s_waitcnt vmcnt(25)
	ds_write_b32 v70, v100
	s_waitcnt vmcnt(24)
	ds_write_b32 v72, v101
	s_waitcnt vmcnt(23)
	ds_write_b32 v74, v102
	s_waitcnt vmcnt(22)
	ds_write_b32 v76, v103
	s_waitcnt vmcnt(21)
	ds_write_b32 v78, v104
	s_waitcnt vmcnt(20)
	ds_write_b32 v80, v105
	s_waitcnt vmcnt(19)
	ds_write_b32 v82, v106
	s_waitcnt vmcnt(18)
	ds_write_b32 v84, v107
	s_waitcnt vmcnt(17)
	ds_write_b32 v86, v108
	s_waitcnt vmcnt(16)
	ds_write_b32 v88, v109
	s_waitcnt vmcnt(15)
	ds_write_b32 v110, v158
	s_waitcnt vmcnt(14)
	ds_write_b32 v124, v159
	s_waitcnt vmcnt(13)
	ds_write_b32 v126, v160
	s_waitcnt vmcnt(12)
	ds_write_b32 v128, v161
	s_waitcnt vmcnt(11)
	ds_write_b32 v130, v162
	s_waitcnt vmcnt(10)
	ds_write_b32 v132, v163
	s_waitcnt vmcnt(9)
	ds_write_b32 v134, v164
	s_waitcnt vmcnt(8)
	ds_write_b32 v136, v165
	s_waitcnt vmcnt(7)
	ds_write_b32 v138, v166
	s_waitcnt vmcnt(6)
	ds_write_b32 v140, v167
	s_waitcnt vmcnt(5)
	ds_write_b32 v142, v168
	s_waitcnt vmcnt(4)
	ds_write_b32 v144, v169
	s_waitcnt vmcnt(3)
	ds_write_b32 v146, v170
	s_waitcnt vmcnt(2)
	ds_write_b32 v148, v171
	s_waitcnt vmcnt(1)
	ds_write_b32 v150, v172
	s_waitcnt vmcnt(0)
	ds_write_b32 v152, v173

.LBB0_185:
	s_lshl_b32 s41, s27, 1
	s_lshl_b32 s42, s20, 1
	v_or_b32_e32 v25, s41, v1
	v_or_b32_e32 v27, s42, v6
	s_add_i32 s43, s41, 4
	s_add_i32 s44, s42, 4
	s_add_i32 s45, s41, 8
	s_add_i32 s46, s42, 8
	s_add_i32 s47, s41, 12
	s_add_i32 s48, s42, 12
	s_add_i32 s49, s41, 16
	s_add_i32 s50, s42, 16
	s_add_i32 s51, s41, 20
	s_add_i32 s52, s42, 20
	s_add_i32 s53, s41, 24
	s_add_i32 s54, s42, 24
	s_add_i32 s41, s41, 28
	s_add_i32 s42, s42, 28
	v_add_u32_e32 v29, s21, v25
	v_add_u32_e32 v4, s26, v27
	v_or_b32_e32 v64, s43, v1
	v_or_b32_e32 v65, s44, v6
	v_or_b32_e32 v66, s45, v1
	v_or_b32_e32 v67, s46, v6
	v_or_b32_e32 v68, s47, v1
	v_or_b32_e32 v69, s48, v6
	v_or_b32_e32 v70, s49, v1
	v_or_b32_e32 v71, s50, v6
	v_or_b32_e32 v72, s51, v1
	v_or_b32_e32 v73, s52, v6
	v_or_b32_e32 v74, s53, v1
	v_or_b32_e32 v75, s54, v6
	v_or_b32_e32 v76, s41, v1
	v_or_b32_e32 v77, s42, v6
	v_mad_i64_i32 v[4:5], s[42:43], v4, s36, v[2:3]
	v_mad_i64_i32 v[30:31], s[42:43], v29, s36, v[2:3]
	v_add_u32_e32 v29, s21, v64
	v_add_u32_e32 v32, s26, v65
	v_add_u32_e32 v42, s21, v66
	v_add_u32_e32 v40, s26, v67
	v_add_u32_e32 v46, s21, v68
	v_add_u32_e32 v44, s26, v69
	v_add_u32_e32 v50, s21, v70
	v_add_u32_e32 v48, s26, v71
	v_add_u32_e32 v54, s21, v72
	v_add_u32_e32 v52, s26, v73
	v_add_u32_e32 v58, s21, v74
	v_add_u32_e32 v56, s26, v75
	v_add_u32_e32 v62, s21, v76
	v_add_u32_e32 v60, s26, v77
	v_mad_i64_i32 v[32:33], s[42:43], v32, s36, v[2:3]
	v_mad_i64_i32 v[34:35], s[42:43], v29, s36, v[2:3]
	v_mad_i64_i32 v[40:41], s[42:43], v40, s36, v[2:3]
	v_mad_i64_i32 v[42:43], s[42:43], v42, s36, v[2:3]
	v_mad_i64_i32 v[44:45], s[42:43], v44, s36, v[2:3]
	v_mad_i64_i32 v[46:47], s[42:43], v46, s36, v[2:3]
	v_mad_i64_i32 v[48:49], s[42:43], v48, s36, v[2:3]
	v_mad_i64_i32 v[50:51], s[42:43], v50, s36, v[2:3]
	v_mad_i64_i32 v[52:53], s[42:43], v52, s36, v[2:3]
	v_mad_i64_i32 v[54:55], s[42:43], v54, s36, v[2:3]
	v_mad_i64_i32 v[56:57], s[42:43], v56, s36, v[2:3]
	v_mad_i64_i32 v[58:59], s[42:43], v58, s36, v[2:3]
	v_mad_i64_i32 v[60:61], s[42:43], v60, s36, v[2:3]
	v_mad_i64_i32 v[62:63], s[42:43], v62, s36, v[2:3]
	global_load_dword v29, v[4:5], off nt
	global_load_dword v78, v[30:31], off nt
	global_load_dword v79, v[32:33], off nt
	global_load_dword v80, v[34:35], off nt
	global_load_dword v81, v[40:41], off nt
	global_load_dword v82, v[42:43], off nt
	global_load_dword v83, v[44:45], off nt
	global_load_dword v84, v[46:47], off nt
	global_load_dword v85, v[48:49], off nt
	global_load_dword v86, v[50:51], off nt
	global_load_dword v87, v[52:53], off nt
	global_load_dword v88, v[54:55], off nt
	global_load_dword v89, v[56:57], off nt
	global_load_dword v90, v[58:59], off nt
	global_load_dword v91, v[60:61], off nt
	global_load_dword v92, v[62:63], off nt
	s_add_i32 s20, s20, 16
	s_add_i32 s27, s27, 16
	s_add_i32 s31, s31, -16
	v_mad_u64_u32 v[4:5], s[42:43], v27, s37, v[10:11]
	s_cmp_lg_u32 s31, 0
	v_mad_u64_u32 v[30:31], s[42:43], v25, s37, v[10:11]
	v_mad_u64_u32 v[32:33], s[42:43], v65, s37, v[10:11]
	v_mad_u64_u32 v[34:35], s[42:43], v64, s37, v[10:11]
	v_mad_u64_u32 v[40:41], s[42:43], v67, s37, v[10:11]
	v_mad_u64_u32 v[42:43], s[42:43], v66, s37, v[10:11]
	v_mad_u64_u32 v[44:45], s[42:43], v69, s37, v[10:11]
	v_mad_u64_u32 v[46:47], s[42:43], v68, s37, v[10:11]
	v_mad_u64_u32 v[48:49], s[42:43], v71, s37, v[10:11]
	v_mad_u64_u32 v[50:51], s[42:43], v70, s37, v[10:11]
	v_mad_u64_u32 v[52:53], s[42:43], v73, s37, v[10:11]
	v_mad_u64_u32 v[54:55], s[42:43], v72, s37, v[10:11]
	v_mad_u64_u32 v[56:57], s[42:43], v75, s37, v[10:11]
	v_mad_u64_u32 v[58:59], s[42:43], v74, s37, v[10:11]
	v_mad_u64_u32 v[60:61], s[42:43], v77, s37, v[10:11]
	v_mad_u64_u32 v[62:63], s[42:43], v76, s37, v[10:11]
	s_lshl_b32 s41, s27, 1
	s_lshl_b32 s42, s20, 1
	v_or_b32_e32 v112, s41, v1
	v_or_b32_e32 v113, s42, v6
	s_add_i32 s43, s41, 4
	s_add_i32 s44, s42, 4
	s_add_i32 s45, s41, 8
	s_add_i32 s46, s42, 8
	s_add_i32 s47, s41, 12
	s_add_i32 s48, s42, 12
	s_add_i32 s49, s41, 16
	s_add_i32 s50, s42, 16
	s_add_i32 s51, s41, 20
	s_add_i32 s52, s42, 20
	s_add_i32 s53, s41, 24
	s_add_i32 s54, s42, 24
	s_add_i32 s41, s41, 28
	s_add_i32 s42, s42, 28
	v_add_u32_e32 v114, s21, v112
	v_add_u32_e32 v110, s26, v113
	v_or_b32_e32 v146, s43, v1
	v_or_b32_e32 v147, s44, v6
	v_or_b32_e32 v148, s45, v1
	v_or_b32_e32 v149, s46, v6
	v_or_b32_e32 v150, s47, v1
	v_or_b32_e32 v151, s48, v6
	v_or_b32_e32 v152, s49, v1
	v_or_b32_e32 v153, s50, v6
	v_or_b32_e32 v154, s51, v1
	v_or_b32_e32 v155, s52, v6
	v_or_b32_e32 v156, s53, v1
	v_or_b32_e32 v157, s54, v6
	v_or_b32_e32 v158, s41, v1
	v_or_b32_e32 v159, s42, v6
	v_mad_i64_i32 v[110:111], s[42:43], v110, s36, v[2:3]
	v_mad_i64_i32 v[116:117], s[42:43], v114, s36, v[2:3]
	v_add_u32_e32 v114, s21, v146
	v_add_u32_e32 v118, s26, v147
	v_add_u32_e32 v124, s21, v148
	v_add_u32_e32 v122, s26, v149
	v_add_u32_e32 v128, s21, v150
	v_add_u32_e32 v126, s26, v151
	v_add_u32_e32 v132, s21, v152
	v_add_u32_e32 v130, s26, v153
	v_add_u32_e32 v136, s21, v154
	v_add_u32_e32 v134, s26, v155
	v_add_u32_e32 v140, s21, v156
	v_add_u32_e32 v138, s26, v157
	v_add_u32_e32 v144, s21, v158
	v_add_u32_e32 v142, s26, v159
	v_mad_i64_i32 v[118:119], s[42:43], v118, s36, v[2:3]
	v_mad_i64_i32 v[120:121], s[42:43], v114, s36, v[2:3]
	v_mad_i64_i32 v[122:123], s[42:43], v122, s36, v[2:3]
	v_mad_i64_i32 v[124:125], s[42:43], v124, s36, v[2:3]
	v_mad_i64_i32 v[126:127], s[42:43], v126, s36, v[2:3]
	v_mad_i64_i32 v[128:129], s[42:43], v128, s36, v[2:3]
	v_mad_i64_i32 v[130:131], s[42:43], v130, s36, v[2:3]
	v_mad_i64_i32 v[132:133], s[42:43], v132, s36, v[2:3]
	v_mad_i64_i32 v[134:135], s[42:43], v134, s36, v[2:3]
	v_mad_i64_i32 v[136:137], s[42:43], v136, s36, v[2:3]
	v_mad_i64_i32 v[138:139], s[42:43], v138, s36, v[2:3]
	v_mad_i64_i32 v[140:141], s[42:43], v140, s36, v[2:3]
	v_mad_i64_i32 v[142:143], s[42:43], v142, s36, v[2:3]
	v_mad_i64_i32 v[144:145], s[42:43], v144, s36, v[2:3]
	global_load_dword v114, v[110:111], off nt
	global_load_dword v160, v[116:117], off nt
	global_load_dword v161, v[118:119], off nt
	global_load_dword v162, v[120:121], off nt
	global_load_dword v163, v[122:123], off nt
	global_load_dword v164, v[124:125], off nt
	global_load_dword v165, v[126:127], off nt
	global_load_dword v166, v[128:129], off nt
	global_load_dword v167, v[130:131], off nt
	global_load_dword v168, v[132:133], off nt
	global_load_dword v169, v[134:135], off nt
	global_load_dword v170, v[136:137], off nt
	global_load_dword v171, v[138:139], off nt
	global_load_dword v172, v[140:141], off nt
	global_load_dword v173, v[142:143], off nt
	global_load_dword v174, v[144:145], off nt
	s_add_i32 s20, s20, 16
	s_add_i32 s27, s27, 16
	s_add_i32 s31, s31, -16
	v_mad_u64_u32 v[110:111], s[42:43], v113, s37, v[10:11]
	s_cmp_lg_u32 s31, 0
	v_mad_u64_u32 v[116:117], s[42:43], v112, s37, v[10:11]
	v_mad_u64_u32 v[118:119], s[42:43], v147, s37, v[10:11]
	v_mad_u64_u32 v[120:121], s[42:43], v146, s37, v[10:11]
	v_mad_u64_u32 v[122:123], s[42:43], v149, s37, v[10:11]
	v_mad_u64_u32 v[124:125], s[42:43], v148, s37, v[10:11]
	v_mad_u64_u32 v[126:127], s[42:43], v151, s37, v[10:11]
	v_mad_u64_u32 v[128:129], s[42:43], v150, s37, v[10:11]
	v_mad_u64_u32 v[130:131], s[42:43], v153, s37, v[10:11]
	v_mad_u64_u32 v[132:133], s[42:43], v152, s37, v[10:11]
	v_mad_u64_u32 v[134:135], s[42:43], v155, s37, v[10:11]
	v_mad_u64_u32 v[136:137], s[42:43], v154, s37, v[10:11]
	v_mad_u64_u32 v[138:139], s[42:43], v157, s37, v[10:11]
	v_mad_u64_u32 v[140:141], s[42:43], v156, s37, v[10:11]
	v_mad_u64_u32 v[142:143], s[42:43], v159, s37, v[10:11]
	v_mad_u64_u32 v[144:145], s[42:43], v158, s37, v[10:11]
	s_waitcnt vmcnt(31)
	ds_write_b32 v4, v29
	s_waitcnt vmcnt(30)
	ds_write_b32 v30, v78
	s_waitcnt vmcnt(29)
	ds_write_b32 v32, v79
	s_waitcnt vmcnt(28)
	ds_write_b32 v34, v80
	s_waitcnt vmcnt(27)
	ds_write_b32 v40, v81
	s_waitcnt vmcnt(26)
	ds_write_b32 v42, v82
	s_waitcnt vmcnt(25)
	ds_write_b32 v44, v83
	s_waitcnt vmcnt(24)
	ds_write_b32 v46, v84
	s_waitcnt vmcnt(23)
	ds_write_b32 v48, v85
	s_waitcnt vmcnt(22)
	ds_write_b32 v50, v86
	s_waitcnt vmcnt(21)
	ds_write_b32 v52, v87
	s_waitcnt vmcnt(20)
	ds_write_b32 v54, v88
	s_waitcnt vmcnt(19)
	ds_write_b32 v56, v89
	s_waitcnt vmcnt(18)
	ds_write_b32 v58, v90
	s_waitcnt vmcnt(17)
	ds_write_b32 v60, v91
	s_waitcnt vmcnt(16)
	ds_write_b32 v62, v92
	s_waitcnt vmcnt(15)
	ds_write_b32 v110, v114
	s_waitcnt vmcnt(14)
	ds_write_b32 v116, v160
	s_waitcnt vmcnt(13)
	ds_write_b32 v118, v161
	s_waitcnt vmcnt(12)
	ds_write_b32 v120, v162
	s_waitcnt vmcnt(11)
	ds_write_b32 v122, v163
	s_waitcnt vmcnt(10)
	ds_write_b32 v124, v164
	s_waitcnt vmcnt(9)
	ds_write_b32 v126, v165
	s_waitcnt vmcnt(8)
	ds_write_b32 v128, v166
	s_waitcnt vmcnt(7)
	ds_write_b32 v130, v167
	s_waitcnt vmcnt(6)
	ds_write_b32 v132, v168
	s_waitcnt vmcnt(5)
	ds_write_b32 v134, v169
	s_waitcnt vmcnt(4)
	ds_write_b32 v136, v170
	s_waitcnt vmcnt(3)
	ds_write_b32 v138, v171
	s_waitcnt vmcnt(2)
	ds_write_b32 v140, v172
	s_waitcnt vmcnt(1)
	ds_write_b32 v142, v173
	s_waitcnt vmcnt(0)
	ds_write_b32 v144, v174

.LBB0_199:
	s_lshl_b32 s38, s21, 1
	s_lshl_b32 s39, s25, 1
	v_or_b32_e32 v25, s38, v1
	v_or_b32_e32 v27, s39, v6
	s_add_i32 s40, s38, 4
	s_add_i32 s41, s39, 4
	s_add_i32 s42, s38, 8
	s_add_i32 s43, s39, 8
	s_add_i32 s44, s38, 12
	s_add_i32 s45, s39, 12
	s_add_i32 s46, s38, 16
	s_add_i32 s47, s39, 16
	s_add_i32 s48, s38, 20
	s_add_i32 s49, s39, 20
	s_add_i32 s50, s38, 24
	s_add_i32 s51, s39, 24
	s_add_i32 s38, s38, 28
	s_add_i32 s39, s39, 28
	v_add_u32_e32 v32, s24, v27
	v_or_b32_e32 v29, s40, v1
	v_or_b32_e32 v66, s41, v6
	v_or_b32_e32 v67, s42, v1
	v_or_b32_e32 v68, s43, v6
	v_or_b32_e32 v69, s44, v1
	v_or_b32_e32 v70, s45, v6
	v_or_b32_e32 v71, s46, v1
	v_or_b32_e32 v72, s47, v6
	v_or_b32_e32 v73, s48, v1
	v_or_b32_e32 v74, s49, v6
	v_or_b32_e32 v75, s50, v1
	v_or_b32_e32 v76, s51, v6
	v_or_b32_e32 v77, s38, v1
	v_or_b32_e32 v78, s39, v6
	v_add_u32_e32 v4, s20, v25
	v_ashrrev_i32_e32 v33, 31, v32
	v_add_u32_e32 v34, s20, v29
	v_add_u32_e32 v40, s24, v66
	v_add_u32_e32 v42, s20, v67
	v_add_u32_e32 v44, s24, v68
	v_add_u32_e32 v46, s20, v69
	v_add_u32_e32 v48, s24, v70
	v_add_u32_e32 v50, s20, v71
	v_add_u32_e32 v52, s24, v72
	v_add_u32_e32 v54, s20, v73
	v_add_u32_e32 v56, s24, v74
	v_add_u32_e32 v58, s20, v75
	v_add_u32_e32 v60, s24, v76
	v_add_u32_e32 v62, s20, v77
	v_add_u32_e32 v64, s24, v78
	v_ashrrev_i32_e32 v5, 31, v4
	v_lshlrev_b64 v[32:33], 12, v[32:33]
	v_ashrrev_i32_e32 v41, 31, v40
	v_ashrrev_i32_e32 v35, 31, v34
	v_ashrrev_i32_e32 v45, 31, v44
	v_ashrrev_i32_e32 v43, 31, v42
	v_ashrrev_i32_e32 v49, 31, v48
	v_ashrrev_i32_e32 v47, 31, v46
	v_ashrrev_i32_e32 v53, 31, v52
	v_ashrrev_i32_e32 v51, 31, v50
	v_ashrrev_i32_e32 v57, 31, v56
	v_ashrrev_i32_e32 v55, 31, v54
	v_ashrrev_i32_e32 v61, 31, v60
	v_ashrrev_i32_e32 v59, 31, v58
	v_ashrrev_i32_e32 v65, 31, v64
	v_ashrrev_i32_e32 v63, 31, v62
	v_lshlrev_b64 v[4:5], 12, v[4:5]
	v_lshl_add_u64 v[32:33], v[2:3], 0, v[32:33]
	v_lshlrev_b64 v[34:35], 12, v[34:35]
	v_lshlrev_b64 v[40:41], 12, v[40:41]
	v_lshlrev_b64 v[42:43], 12, v[42:43]
	v_lshlrev_b64 v[44:45], 12, v[44:45]
	v_lshlrev_b64 v[46:47], 12, v[46:47]
	v_lshlrev_b64 v[48:49], 12, v[48:49]
	v_lshlrev_b64 v[50:51], 12, v[50:51]
	v_lshlrev_b64 v[52:53], 12, v[52:53]
	v_lshlrev_b64 v[54:55], 12, v[54:55]
	v_lshlrev_b64 v[56:57], 12, v[56:57]
	v_lshlrev_b64 v[58:59], 12, v[58:59]
	v_lshlrev_b64 v[60:61], 12, v[60:61]
	v_lshlrev_b64 v[62:63], 12, v[62:63]
	v_lshlrev_b64 v[64:65], 12, v[64:65]
	v_lshl_add_u64 v[4:5], v[2:3], 0, v[4:5]
	v_lshl_add_u64 v[40:41], v[2:3], 0, v[40:41]
	v_lshl_add_u64 v[34:35], v[2:3], 0, v[34:35]
	v_lshl_add_u64 v[44:45], v[2:3], 0, v[44:45]
	v_lshl_add_u64 v[42:43], v[2:3], 0, v[42:43]
	v_lshl_add_u64 v[48:49], v[2:3], 0, v[48:49]
	v_lshl_add_u64 v[46:47], v[2:3], 0, v[46:47]
	v_lshl_add_u64 v[52:53], v[2:3], 0, v[52:53]
	v_lshl_add_u64 v[50:51], v[2:3], 0, v[50:51]
	v_lshl_add_u64 v[56:57], v[2:3], 0, v[56:57]
	v_lshl_add_u64 v[54:55], v[2:3], 0, v[54:55]
	v_lshl_add_u64 v[60:61], v[2:3], 0, v[60:61]
	v_lshl_add_u64 v[58:59], v[2:3], 0, v[58:59]
	v_lshl_add_u64 v[64:65], v[2:3], 0, v[64:65]
	v_lshl_add_u64 v[62:63], v[2:3], 0, v[62:63]
	global_load_dword v79, v[32:33], off nt
	global_load_dword v80, v[4:5], off nt
	global_load_dword v81, v[40:41], off nt
	global_load_dword v82, v[34:35], off nt
	global_load_dword v83, v[44:45], off nt
	global_load_dword v84, v[42:43], off nt
	global_load_dword v85, v[48:49], off nt
	global_load_dword v86, v[46:47], off nt
	global_load_dword v87, v[52:53], off nt
	global_load_dword v88, v[50:51], off nt
	global_load_dword v89, v[56:57], off nt
	global_load_dword v90, v[54:55], off nt
	global_load_dword v91, v[60:61], off nt
	global_load_dword v92, v[58:59], off nt
	global_load_dword v93, v[64:65], off nt
	global_load_dword v94, v[62:63], off nt
	s_add_i32 s25, s25, 16
	s_add_i32 s21, s21, 16
	s_add_i32 s31, s31, -16
	v_mad_u64_u32 v[4:5], s[38:39], v27, s37, v[10:11]
	s_cmp_lg_u32 s31, 0
	v_mad_u64_u32 v[32:33], s[38:39], v25, s37, v[10:11]
	v_mad_u64_u32 v[34:35], s[38:39], v66, s37, v[10:11]
	v_mad_u64_u32 v[40:41], s[38:39], v29, s37, v[10:11]
	v_mad_u64_u32 v[42:43], s[38:39], v68, s37, v[10:11]
	v_mad_u64_u32 v[44:45], s[38:39], v67, s37, v[10:11]
	v_mad_u64_u32 v[46:47], s[38:39], v70, s37, v[10:11]
	v_mad_u64_u32 v[48:49], s[38:39], v69, s37, v[10:11]
	v_mad_u64_u32 v[50:51], s[38:39], v72, s37, v[10:11]
	v_mad_u64_u32 v[52:53], s[38:39], v71, s37, v[10:11]
	v_mad_u64_u32 v[54:55], s[38:39], v74, s37, v[10:11]
	v_mad_u64_u32 v[56:57], s[38:39], v73, s37, v[10:11]
	v_mad_u64_u32 v[58:59], s[38:39], v76, s37, v[10:11]
	v_mad_u64_u32 v[60:61], s[38:39], v75, s37, v[10:11]
	v_mad_u64_u32 v[62:63], s[38:39], v78, s37, v[10:11]
	v_mad_u64_u32 v[64:65], s[38:39], v77, s37, v[10:11]
	s_lshl_b32 s38, s21, 1
	s_lshl_b32 s39, s25, 1
	v_or_b32_e32 v112, s38, v1
	v_or_b32_e32 v113, s39, v6
	s_add_i32 s40, s38, 4
	s_add_i32 s41, s39, 4
	s_add_i32 s42, s38, 8
	s_add_i32 s43, s39, 8
	s_add_i32 s44, s38, 12
	s_add_i32 s45, s39, 12
	s_add_i32 s46, s38, 16
	s_add_i32 s47, s39, 16
	s_add_i32 s48, s38, 20
	s_add_i32 s49, s39, 20
	s_add_i32 s50, s38, 24
	s_add_i32 s51, s39, 24
	s_add_i32 s38, s38, 28
	s_add_i32 s39, s39, 28
	v_add_u32_e32 v116, s24, v113
	v_or_b32_e32 v114, s40, v1
	v_or_b32_e32 v146, s41, v6
	v_or_b32_e32 v147, s42, v1
	v_or_b32_e32 v148, s43, v6
	v_or_b32_e32 v149, s44, v1
	v_or_b32_e32 v150, s45, v6
	v_or_b32_e32 v151, s46, v1
	v_or_b32_e32 v152, s47, v6
	v_or_b32_e32 v153, s48, v1
	v_or_b32_e32 v154, s49, v6
	v_or_b32_e32 v155, s50, v1
	v_or_b32_e32 v156, s51, v6
	v_or_b32_e32 v157, s38, v1
	v_or_b32_e32 v158, s39, v6
	v_add_u32_e32 v110, s20, v112
	v_ashrrev_i32_e32 v117, 31, v116
	v_add_u32_e32 v118, s20, v114
	v_add_u32_e32 v120, s24, v146
	v_add_u32_e32 v122, s20, v147
	v_add_u32_e32 v124, s24, v148
	v_add_u32_e32 v126, s20, v149
	v_add_u32_e32 v128, s24, v150
	v_add_u32_e32 v130, s20, v151
	v_add_u32_e32 v132, s24, v152
	v_add_u32_e32 v134, s20, v153
	v_add_u32_e32 v136, s24, v154
	v_add_u32_e32 v138, s20, v155
	v_add_u32_e32 v140, s24, v156
	v_add_u32_e32 v142, s20, v157
	v_add_u32_e32 v144, s24, v158
	v_ashrrev_i32_e32 v111, 31, v110
	v_lshlrev_b64 v[116:117], 12, v[116:117]
	v_ashrrev_i32_e32 v121, 31, v120
	v_ashrrev_i32_e32 v119, 31, v118
	v_ashrrev_i32_e32 v125, 31, v124
	v_ashrrev_i32_e32 v123, 31, v122
	v_ashrrev_i32_e32 v129, 31, v128
	v_ashrrev_i32_e32 v127, 31, v126
	v_ashrrev_i32_e32 v133, 31, v132
	v_ashrrev_i32_e32 v131, 31, v130
	v_ashrrev_i32_e32 v137, 31, v136
	v_ashrrev_i32_e32 v135, 31, v134
	v_ashrrev_i32_e32 v141, 31, v140
	v_ashrrev_i32_e32 v139, 31, v138
	v_ashrrev_i32_e32 v145, 31, v144
	v_ashrrev_i32_e32 v143, 31, v142
	v_lshlrev_b64 v[110:111], 12, v[110:111]
	v_lshl_add_u64 v[116:117], v[2:3], 0, v[116:117]
	v_lshlrev_b64 v[118:119], 12, v[118:119]
	v_lshlrev_b64 v[120:121], 12, v[120:121]
	v_lshlrev_b64 v[122:123], 12, v[122:123]
	v_lshlrev_b64 v[124:125], 12, v[124:125]
	v_lshlrev_b64 v[126:127], 12, v[126:127]
	v_lshlrev_b64 v[128:129], 12, v[128:129]
	v_lshlrev_b64 v[130:131], 12, v[130:131]
	v_lshlrev_b64 v[132:133], 12, v[132:133]
	v_lshlrev_b64 v[134:135], 12, v[134:135]
	v_lshlrev_b64 v[136:137], 12, v[136:137]
	v_lshlrev_b64 v[138:139], 12, v[138:139]
	v_lshlrev_b64 v[140:141], 12, v[140:141]
	v_lshlrev_b64 v[142:143], 12, v[142:143]
	v_lshlrev_b64 v[144:145], 12, v[144:145]
	v_lshl_add_u64 v[110:111], v[2:3], 0, v[110:111]
	v_lshl_add_u64 v[120:121], v[2:3], 0, v[120:121]
	v_lshl_add_u64 v[118:119], v[2:3], 0, v[118:119]
	v_lshl_add_u64 v[124:125], v[2:3], 0, v[124:125]
	v_lshl_add_u64 v[122:123], v[2:3], 0, v[122:123]
	v_lshl_add_u64 v[128:129], v[2:3], 0, v[128:129]
	v_lshl_add_u64 v[126:127], v[2:3], 0, v[126:127]
	v_lshl_add_u64 v[132:133], v[2:3], 0, v[132:133]
	v_lshl_add_u64 v[130:131], v[2:3], 0, v[130:131]
	v_lshl_add_u64 v[136:137], v[2:3], 0, v[136:137]
	v_lshl_add_u64 v[134:135], v[2:3], 0, v[134:135]
	v_lshl_add_u64 v[140:141], v[2:3], 0, v[140:141]
	v_lshl_add_u64 v[138:139], v[2:3], 0, v[138:139]
	v_lshl_add_u64 v[144:145], v[2:3], 0, v[144:145]
	v_lshl_add_u64 v[142:143], v[2:3], 0, v[142:143]
	global_load_dword v159, v[116:117], off nt
	global_load_dword v160, v[110:111], off nt
	global_load_dword v161, v[120:121], off nt
	global_load_dword v162, v[118:119], off nt
	global_load_dword v163, v[124:125], off nt
	global_load_dword v164, v[122:123], off nt
	global_load_dword v165, v[128:129], off nt
	global_load_dword v166, v[126:127], off nt
	global_load_dword v167, v[132:133], off nt
	global_load_dword v168, v[130:131], off nt
	global_load_dword v169, v[136:137], off nt
	global_load_dword v170, v[134:135], off nt
	global_load_dword v171, v[140:141], off nt
	global_load_dword v172, v[138:139], off nt
	global_load_dword v173, v[144:145], off nt
	global_load_dword v174, v[142:143], off nt
	s_add_i32 s25, s25, 16
	s_add_i32 s21, s21, 16
	s_add_i32 s31, s31, -16
	v_mad_u64_u32 v[110:111], s[38:39], v113, s37, v[10:11]
	s_cmp_lg_u32 s31, 0
	v_mad_u64_u32 v[116:117], s[38:39], v112, s37, v[10:11]
	v_mad_u64_u32 v[118:119], s[38:39], v146, s37, v[10:11]
	v_mad_u64_u32 v[120:121], s[38:39], v114, s37, v[10:11]
	v_mad_u64_u32 v[122:123], s[38:39], v148, s37, v[10:11]
	v_mad_u64_u32 v[124:125], s[38:39], v147, s37, v[10:11]
	v_mad_u64_u32 v[126:127], s[38:39], v150, s37, v[10:11]
	v_mad_u64_u32 v[128:129], s[38:39], v149, s37, v[10:11]
	v_mad_u64_u32 v[130:131], s[38:39], v152, s37, v[10:11]
	v_mad_u64_u32 v[132:133], s[38:39], v151, s37, v[10:11]
	v_mad_u64_u32 v[134:135], s[38:39], v154, s37, v[10:11]
	v_mad_u64_u32 v[136:137], s[38:39], v153, s37, v[10:11]
	v_mad_u64_u32 v[138:139], s[38:39], v156, s37, v[10:11]
	v_mad_u64_u32 v[140:141], s[38:39], v155, s37, v[10:11]
	v_mad_u64_u32 v[142:143], s[38:39], v158, s37, v[10:11]
	v_mad_u64_u32 v[144:145], s[38:39], v157, s37, v[10:11]
	s_waitcnt vmcnt(31)
	ds_write_b32 v4, v79
	s_waitcnt vmcnt(30)
	ds_write_b32 v32, v80
	s_waitcnt vmcnt(29)
	ds_write_b32 v34, v81
	s_waitcnt vmcnt(28)
	ds_write_b32 v40, v82
	s_waitcnt vmcnt(27)
	ds_write_b32 v42, v83
	s_waitcnt vmcnt(26)
	ds_write_b32 v44, v84
	s_waitcnt vmcnt(25)
	ds_write_b32 v46, v85
	s_waitcnt vmcnt(24)
	ds_write_b32 v48, v86
	s_waitcnt vmcnt(23)
	ds_write_b32 v50, v87
	s_waitcnt vmcnt(22)
	ds_write_b32 v52, v88
	s_waitcnt vmcnt(21)
	ds_write_b32 v54, v89
	s_waitcnt vmcnt(20)
	ds_write_b32 v56, v90
	s_waitcnt vmcnt(19)
	ds_write_b32 v58, v91
	s_waitcnt vmcnt(18)
	ds_write_b32 v60, v92
	s_waitcnt vmcnt(17)
	ds_write_b32 v62, v93
	s_waitcnt vmcnt(16)
	ds_write_b32 v64, v94
	s_waitcnt vmcnt(15)
	ds_write_b32 v110, v159
	s_waitcnt vmcnt(14)
	ds_write_b32 v116, v160
	s_waitcnt vmcnt(13)
	ds_write_b32 v118, v161
	s_waitcnt vmcnt(12)
	ds_write_b32 v120, v162
	s_waitcnt vmcnt(11)
	ds_write_b32 v122, v163
	s_waitcnt vmcnt(10)
	ds_write_b32 v124, v164
	s_waitcnt vmcnt(9)
	ds_write_b32 v126, v165
	s_waitcnt vmcnt(8)
	ds_write_b32 v128, v166
	s_waitcnt vmcnt(7)
	ds_write_b32 v130, v167
	s_waitcnt vmcnt(6)
	ds_write_b32 v132, v168
	s_waitcnt vmcnt(5)
	ds_write_b32 v134, v169
	s_waitcnt vmcnt(4)
	ds_write_b32 v136, v170
	s_waitcnt vmcnt(3)
	ds_write_b32 v138, v171
	s_waitcnt vmcnt(2)
	ds_write_b32 v140, v172
	s_waitcnt vmcnt(1)
	ds_write_b32 v142, v173
	s_waitcnt vmcnt(0)
	ds_write_b32 v144, v174

.LBB0_215:
	s_lshl_b32 s40, s38, 1
	s_lshl_b32 s41, s19, 1
	v_or_b32_e32 v11, s40, v1
	v_or_b32_e32 v64, s41, v6
	s_add_i32 s42, s40, 4
	s_add_i32 s43, s41, 4
	s_add_i32 s44, s40, 8
	s_add_i32 s45, s41, 8
	s_add_i32 s46, s40, 12
	s_add_i32 s47, s41, 12
	s_add_i32 s48, s40, 16
	s_add_i32 s49, s41, 16
	s_add_i32 s50, s40, 20
	s_add_i32 s51, s41, 20
	s_add_i32 s52, s40, 24
	s_add_i32 s53, s41, 24
	s_add_i32 s40, s40, 28
	s_add_i32 s41, s41, 28
	v_add_u32_e32 v4, s18, v64
	v_or_b32_e32 v65, s42, v1
	v_or_b32_e32 v66, s43, v6
	v_or_b32_e32 v67, s44, v1
	v_or_b32_e32 v68, s45, v6
	v_or_b32_e32 v69, s46, v1
	v_or_b32_e32 v70, s47, v6
	v_or_b32_e32 v71, s48, v1
	v_or_b32_e32 v72, s49, v6
	v_or_b32_e32 v73, s50, v1
	v_or_b32_e32 v74, s51, v6
	v_or_b32_e32 v75, s52, v1
	v_or_b32_e32 v76, s53, v6
	v_or_b32_e32 v77, s40, v1
	v_or_b32_e32 v78, s41, v6
	v_add_u32_e32 v30, s23, v11
	v_mad_i64_i32 v[4:5], s[40:41], v4, s30, v[2:3]
	v_add_u32_e32 v34, s23, v65
	v_add_u32_e32 v32, s18, v66
	v_add_u32_e32 v42, s23, v67
	v_add_u32_e32 v40, s18, v68
	v_add_u32_e32 v46, s23, v69
	v_add_u32_e32 v44, s18, v70
	v_add_u32_e32 v50, s23, v71
	v_add_u32_e32 v48, s18, v72
	v_add_u32_e32 v54, s23, v73
	v_add_u32_e32 v52, s18, v74
	v_add_u32_e32 v58, s23, v75
	v_add_u32_e32 v56, s18, v76
	v_add_u32_e32 v62, s23, v77
	v_add_u32_e32 v60, s18, v78
	v_mad_i64_i32 v[30:31], s[40:41], v30, s30, v[2:3]
	v_mad_i64_i32 v[32:33], s[40:41], v32, s30, v[2:3]
	v_mad_i64_i32 v[34:35], s[40:41], v34, s30, v[2:3]
	v_mad_i64_i32 v[40:41], s[40:41], v40, s30, v[2:3]
	v_mad_i64_i32 v[42:43], s[40:41], v42, s30, v[2:3]
	v_mad_i64_i32 v[44:45], s[40:41], v44, s30, v[2:3]
	v_mad_i64_i32 v[46:47], s[40:41], v46, s30, v[2:3]
	v_mad_i64_i32 v[48:49], s[40:41], v48, s30, v[2:3]
	v_mad_i64_i32 v[50:51], s[40:41], v50, s30, v[2:3]
	v_mad_i64_i32 v[52:53], s[40:41], v52, s30, v[2:3]
	v_mad_i64_i32 v[54:55], s[40:41], v54, s30, v[2:3]
	v_mad_i64_i32 v[56:57], s[40:41], v56, s30, v[2:3]
	v_mad_i64_i32 v[58:59], s[40:41], v58, s30, v[2:3]
	v_mad_i64_i32 v[60:61], s[40:41], v60, s30, v[2:3]
	v_mad_i64_i32 v[62:63], s[40:41], v62, s30, v[2:3]
	global_load_dword v79, v[4:5], off nt
	global_load_dword v80, v[30:31], off nt
	global_load_dword v81, v[32:33], off nt
	global_load_dword v82, v[34:35], off nt
	global_load_dword v83, v[40:41], off nt
	global_load_dword v84, v[42:43], off nt
	global_load_dword v85, v[44:45], off nt
	global_load_dword v86, v[46:47], off nt
	global_load_dword v87, v[48:49], off nt
	global_load_dword v88, v[50:51], off nt
	global_load_dword v89, v[52:53], off nt
	global_load_dword v90, v[54:55], off nt
	global_load_dword v91, v[56:57], off nt
	global_load_dword v92, v[58:59], off nt
	global_load_dword v93, v[60:61], off nt
	global_load_dword v94, v[62:63], off nt
	s_add_i32 s19, s19, 16
	s_add_i32 s38, s38, 16
	s_add_i32 s39, s39, -16
	v_mad_u64_u32 v[4:5], s[40:41], v64, s31, v[10:11]
	s_cmp_lg_u32 s39, 0
	v_mad_u64_u32 v[30:31], s[40:41], v11, s31, v[10:11]
	v_mad_u64_u32 v[32:33], s[40:41], v66, s31, v[10:11]
	v_mad_u64_u32 v[34:35], s[40:41], v65, s31, v[10:11]
	v_mad_u64_u32 v[40:41], s[40:41], v68, s31, v[10:11]
	v_mad_u64_u32 v[42:43], s[40:41], v67, s31, v[10:11]
	v_mad_u64_u32 v[44:45], s[40:41], v70, s31, v[10:11]
	v_mad_u64_u32 v[46:47], s[40:41], v69, s31, v[10:11]
	v_mad_u64_u32 v[48:49], s[40:41], v72, s31, v[10:11]
	v_mad_u64_u32 v[50:51], s[40:41], v71, s31, v[10:11]
	v_mad_u64_u32 v[52:53], s[40:41], v74, s31, v[10:11]
	v_mad_u64_u32 v[54:55], s[40:41], v73, s31, v[10:11]
	v_mad_u64_u32 v[56:57], s[40:41], v76, s31, v[10:11]
	v_mad_u64_u32 v[58:59], s[40:41], v75, s31, v[10:11]
	v_mad_u64_u32 v[60:61], s[40:41], v78, s31, v[10:11]
	v_mad_u64_u32 v[62:63], s[40:41], v77, s31, v[10:11]
	s_lshl_b32 s40, s38, 1
	s_lshl_b32 s41, s19, 1
	v_or_b32_e32 v112, s40, v1
	v_or_b32_e32 v144, s41, v6
	s_add_i32 s42, s40, 4
	s_add_i32 s43, s41, 4
	s_add_i32 s44, s40, 8
	s_add_i32 s45, s41, 8
	s_add_i32 s46, s40, 12
	s_add_i32 s47, s41, 12
	s_add_i32 s48, s40, 16
	s_add_i32 s49, s41, 16
	s_add_i32 s50, s40, 20
	s_add_i32 s51, s41, 20
	s_add_i32 s52, s40, 24
	s_add_i32 s53, s41, 24
	s_add_i32 s40, s40, 28
	s_add_i32 s41, s41, 28
	v_add_u32_e32 v110, s18, v144
	v_or_b32_e32 v145, s42, v1
	v_or_b32_e32 v146, s43, v6
	v_or_b32_e32 v147, s44, v1
	v_or_b32_e32 v148, s45, v6
	v_or_b32_e32 v149, s46, v1
	v_or_b32_e32 v150, s47, v6
	v_or_b32_e32 v151, s48, v1
	v_or_b32_e32 v152, s49, v6
	v_or_b32_e32 v153, s50, v1
	v_or_b32_e32 v154, s51, v6
	v_or_b32_e32 v155, s52, v1
	v_or_b32_e32 v156, s53, v6
	v_or_b32_e32 v157, s40, v1
	v_or_b32_e32 v158, s41, v6
	v_add_u32_e32 v114, s23, v112
	v_mad_i64_i32 v[110:111], s[40:41], v110, s30, v[2:3]
	v_add_u32_e32 v118, s23, v145
	v_add_u32_e32 v116, s18, v146
	v_add_u32_e32 v122, s23, v147
	v_add_u32_e32 v120, s18, v148
	v_add_u32_e32 v126, s23, v149
	v_add_u32_e32 v124, s18, v150
	v_add_u32_e32 v130, s23, v151
	v_add_u32_e32 v128, s18, v152
	v_add_u32_e32 v134, s23, v153
	v_add_u32_e32 v132, s18, v154
	v_add_u32_e32 v138, s23, v155
	v_add_u32_e32 v136, s18, v156
	v_add_u32_e32 v142, s23, v157
	v_add_u32_e32 v140, s18, v158
	v_mad_i64_i32 v[114:115], s[40:41], v114, s30, v[2:3]
	v_mad_i64_i32 v[116:117], s[40:41], v116, s30, v[2:3]
	v_mad_i64_i32 v[118:119], s[40:41], v118, s30, v[2:3]
	v_mad_i64_i32 v[120:121], s[40:41], v120, s30, v[2:3]
	v_mad_i64_i32 v[122:123], s[40:41], v122, s30, v[2:3]
	v_mad_i64_i32 v[124:125], s[40:41], v124, s30, v[2:3]
	v_mad_i64_i32 v[126:127], s[40:41], v126, s30, v[2:3]
	v_mad_i64_i32 v[128:129], s[40:41], v128, s30, v[2:3]
	v_mad_i64_i32 v[130:131], s[40:41], v130, s30, v[2:3]
	v_mad_i64_i32 v[132:133], s[40:41], v132, s30, v[2:3]
	v_mad_i64_i32 v[134:135], s[40:41], v134, s30, v[2:3]
	v_mad_i64_i32 v[136:137], s[40:41], v136, s30, v[2:3]
	v_mad_i64_i32 v[138:139], s[40:41], v138, s30, v[2:3]
	v_mad_i64_i32 v[140:141], s[40:41], v140, s30, v[2:3]
	v_mad_i64_i32 v[142:143], s[40:41], v142, s30, v[2:3]
	global_load_dword v159, v[110:111], off nt
	global_load_dword v160, v[114:115], off nt
	global_load_dword v161, v[116:117], off nt
	global_load_dword v162, v[118:119], off nt
	global_load_dword v163, v[120:121], off nt
	global_load_dword v164, v[122:123], off nt
	global_load_dword v165, v[124:125], off nt
	global_load_dword v166, v[126:127], off nt
	global_load_dword v167, v[128:129], off nt
	global_load_dword v168, v[130:131], off nt
	global_load_dword v169, v[132:133], off nt
	global_load_dword v170, v[134:135], off nt
	global_load_dword v171, v[136:137], off nt
	global_load_dword v172, v[138:139], off nt
	global_load_dword v173, v[140:141], off nt
	global_load_dword v174, v[142:143], off nt
	s_add_i32 s19, s19, 16
	s_add_i32 s38, s38, 16
	s_add_i32 s39, s39, -16
	v_mad_u64_u32 v[110:111], s[40:41], v144, s31, v[10:11]
	s_cmp_lg_u32 s39, 0
	v_mad_u64_u32 v[114:115], s[40:41], v112, s31, v[10:11]
	v_mad_u64_u32 v[116:117], s[40:41], v146, s31, v[10:11]
	v_mad_u64_u32 v[118:119], s[40:41], v145, s31, v[10:11]
	v_mad_u64_u32 v[120:121], s[40:41], v148, s31, v[10:11]
	v_mad_u64_u32 v[122:123], s[40:41], v147, s31, v[10:11]
	v_mad_u64_u32 v[124:125], s[40:41], v150, s31, v[10:11]
	v_mad_u64_u32 v[126:127], s[40:41], v149, s31, v[10:11]
	v_mad_u64_u32 v[128:129], s[40:41], v152, s31, v[10:11]
	v_mad_u64_u32 v[130:131], s[40:41], v151, s31, v[10:11]
	v_mad_u64_u32 v[132:133], s[40:41], v154, s31, v[10:11]
	v_mad_u64_u32 v[134:135], s[40:41], v153, s31, v[10:11]
	v_mad_u64_u32 v[136:137], s[40:41], v156, s31, v[10:11]
	v_mad_u64_u32 v[138:139], s[40:41], v155, s31, v[10:11]
	v_mad_u64_u32 v[140:141], s[40:41], v158, s31, v[10:11]
	v_mad_u64_u32 v[142:143], s[40:41], v157, s31, v[10:11]
	s_waitcnt vmcnt(31)
	ds_write_b32 v4, v79
	s_waitcnt vmcnt(30)
	ds_write_b32 v30, v80
	s_waitcnt vmcnt(29)
	ds_write_b32 v32, v81
	s_waitcnt vmcnt(28)
	ds_write_b32 v34, v82
	s_waitcnt vmcnt(27)
	ds_write_b32 v40, v83
	s_waitcnt vmcnt(26)
	ds_write_b32 v42, v84
	s_waitcnt vmcnt(25)
	ds_write_b32 v44, v85
	s_waitcnt vmcnt(24)
	ds_write_b32 v46, v86
	s_waitcnt vmcnt(23)
	ds_write_b32 v48, v87
	s_waitcnt vmcnt(22)
	ds_write_b32 v50, v88
	s_waitcnt vmcnt(21)
	ds_write_b32 v52, v89
	s_waitcnt vmcnt(20)
	ds_write_b32 v54, v90
	s_waitcnt vmcnt(19)
	ds_write_b32 v56, v91
	s_waitcnt vmcnt(18)
	ds_write_b32 v58, v92
	s_waitcnt vmcnt(17)
	ds_write_b32 v60, v93
	s_waitcnt vmcnt(16)
	ds_write_b32 v62, v94
	s_waitcnt vmcnt(15)
	ds_write_b32 v110, v159
	s_waitcnt vmcnt(14)
	ds_write_b32 v114, v160
	s_waitcnt vmcnt(13)
	ds_write_b32 v116, v161
	s_waitcnt vmcnt(12)
	ds_write_b32 v118, v162
	s_waitcnt vmcnt(11)
	ds_write_b32 v120, v163
	s_waitcnt vmcnt(10)
	ds_write_b32 v122, v164
	s_waitcnt vmcnt(9)
	ds_write_b32 v124, v165
	s_waitcnt vmcnt(8)
	ds_write_b32 v126, v166
	s_waitcnt vmcnt(7)
	ds_write_b32 v128, v167
	s_waitcnt vmcnt(6)
	ds_write_b32 v130, v168
	s_waitcnt vmcnt(5)
	ds_write_b32 v132, v169
	s_waitcnt vmcnt(4)
	ds_write_b32 v134, v170
	s_waitcnt vmcnt(3)
	ds_write_b32 v136, v171
	s_waitcnt vmcnt(2)
	ds_write_b32 v138, v172
	s_waitcnt vmcnt(1)
	ds_write_b32 v140, v173
	s_waitcnt vmcnt(0)
	ds_write_b32 v142, v174

.LBB0_229:
	s_lshl_b32 s36, s33, 1
	s_lshl_b32 s37, s34, 1
	v_or_b32_e32 v11, s36, v1
	v_or_b32_e32 v66, s37, v6
	s_add_i32 s38, s36, 4
	s_add_i32 s39, s37, 4
	s_add_i32 s40, s36, 8
	s_add_i32 s41, s37, 8
	s_add_i32 s42, s36, 12
	s_add_i32 s43, s37, 12
	s_add_i32 s44, s36, 16
	s_add_i32 s45, s37, 16
	s_add_i32 s46, s36, 20
	s_add_i32 s47, s37, 20
	s_add_i32 s48, s36, 24
	s_add_i32 s49, s37, 24
	s_add_i32 s36, s36, 28
	s_add_i32 s37, s37, 28
	v_add_u32_e32 v32, s16, v66
	v_or_b32_e32 v67, s38, v1
	v_or_b32_e32 v68, s39, v6
	v_or_b32_e32 v69, s40, v1
	v_or_b32_e32 v70, s41, v6
	v_or_b32_e32 v71, s42, v1
	v_or_b32_e32 v72, s43, v6
	v_or_b32_e32 v73, s44, v1
	v_or_b32_e32 v74, s45, v6
	v_or_b32_e32 v75, s46, v1
	v_or_b32_e32 v76, s47, v6
	v_or_b32_e32 v77, s48, v1
	v_or_b32_e32 v78, s49, v6
	v_or_b32_e32 v79, s36, v1
	v_or_b32_e32 v80, s37, v6
	v_add_u32_e32 v4, s23, v11
	v_ashrrev_i32_e32 v33, 31, v32
	v_add_u32_e32 v34, s23, v67
	v_add_u32_e32 v40, s16, v68
	v_add_u32_e32 v42, s23, v69
	v_add_u32_e32 v44, s16, v70
	v_add_u32_e32 v46, s23, v71
	v_add_u32_e32 v48, s16, v72
	v_add_u32_e32 v50, s23, v73
	v_add_u32_e32 v52, s16, v74
	v_add_u32_e32 v54, s23, v75
	v_add_u32_e32 v56, s16, v76
	v_add_u32_e32 v58, s23, v77
	v_add_u32_e32 v60, s16, v78
	v_add_u32_e32 v62, s23, v79
	v_add_u32_e32 v64, s16, v80
	v_ashrrev_i32_e32 v5, 31, v4
	v_lshlrev_b64 v[32:33], 12, v[32:33]
	v_ashrrev_i32_e32 v41, 31, v40
	v_ashrrev_i32_e32 v35, 31, v34
	v_ashrrev_i32_e32 v45, 31, v44
	v_ashrrev_i32_e32 v43, 31, v42
	v_ashrrev_i32_e32 v49, 31, v48
	v_ashrrev_i32_e32 v47, 31, v46
	v_ashrrev_i32_e32 v53, 31, v52
	v_ashrrev_i32_e32 v51, 31, v50
	v_ashrrev_i32_e32 v57, 31, v56
	v_ashrrev_i32_e32 v55, 31, v54
	v_ashrrev_i32_e32 v61, 31, v60
	v_ashrrev_i32_e32 v59, 31, v58
	v_ashrrev_i32_e32 v65, 31, v64
	v_ashrrev_i32_e32 v63, 31, v62
	v_lshlrev_b64 v[4:5], 12, v[4:5]
	v_lshl_add_u64 v[32:33], v[2:3], 0, v[32:33]
	v_lshlrev_b64 v[34:35], 12, v[34:35]
	v_lshlrev_b64 v[40:41], 12, v[40:41]
	v_lshlrev_b64 v[42:43], 12, v[42:43]
	v_lshlrev_b64 v[44:45], 12, v[44:45]
	v_lshlrev_b64 v[46:47], 12, v[46:47]
	v_lshlrev_b64 v[48:49], 12, v[48:49]
	v_lshlrev_b64 v[50:51], 12, v[50:51]
	v_lshlrev_b64 v[52:53], 12, v[52:53]
	v_lshlrev_b64 v[54:55], 12, v[54:55]
	v_lshlrev_b64 v[56:57], 12, v[56:57]
	v_lshlrev_b64 v[58:59], 12, v[58:59]
	v_lshlrev_b64 v[60:61], 12, v[60:61]
	v_lshlrev_b64 v[62:63], 12, v[62:63]
	v_lshlrev_b64 v[64:65], 12, v[64:65]
	v_lshl_add_u64 v[4:5], v[2:3], 0, v[4:5]
	v_lshl_add_u64 v[40:41], v[2:3], 0, v[40:41]
	v_lshl_add_u64 v[34:35], v[2:3], 0, v[34:35]
	v_lshl_add_u64 v[44:45], v[2:3], 0, v[44:45]
	v_lshl_add_u64 v[42:43], v[2:3], 0, v[42:43]
	v_lshl_add_u64 v[48:49], v[2:3], 0, v[48:49]
	v_lshl_add_u64 v[46:47], v[2:3], 0, v[46:47]
	v_lshl_add_u64 v[52:53], v[2:3], 0, v[52:53]
	v_lshl_add_u64 v[50:51], v[2:3], 0, v[50:51]
	v_lshl_add_u64 v[56:57], v[2:3], 0, v[56:57]
	v_lshl_add_u64 v[54:55], v[2:3], 0, v[54:55]
	v_lshl_add_u64 v[60:61], v[2:3], 0, v[60:61]
	v_lshl_add_u64 v[58:59], v[2:3], 0, v[58:59]
	v_lshl_add_u64 v[64:65], v[2:3], 0, v[64:65]
	v_lshl_add_u64 v[62:63], v[2:3], 0, v[62:63]
	global_load_dword v81, v[32:33], off nt
	global_load_dword v82, v[4:5], off nt
	global_load_dword v83, v[40:41], off nt
	global_load_dword v84, v[34:35], off nt
	global_load_dword v85, v[44:45], off nt
	global_load_dword v86, v[42:43], off nt
	global_load_dword v87, v[48:49], off nt
	global_load_dword v88, v[46:47], off nt
	global_load_dword v89, v[52:53], off nt
	global_load_dword v90, v[50:51], off nt
	global_load_dword v91, v[56:57], off nt
	global_load_dword v92, v[54:55], off nt
	global_load_dword v93, v[60:61], off nt
	global_load_dword v94, v[58:59], off nt
	global_load_dword v95, v[64:65], off nt
	global_load_dword v96, v[62:63], off nt
	s_add_i32 s34, s34, 16
	s_add_i32 s33, s33, 16
	s_add_i32 s35, s35, -16
	v_mad_u64_u32 v[4:5], s[36:37], v66, s31, v[10:11]
	s_cmp_lg_u32 s35, 0
	v_mad_u64_u32 v[32:33], s[36:37], v11, s31, v[10:11]
	v_mad_u64_u32 v[34:35], s[36:37], v68, s31, v[10:11]
	v_mad_u64_u32 v[40:41], s[36:37], v67, s31, v[10:11]
	v_mad_u64_u32 v[42:43], s[36:37], v70, s31, v[10:11]
	v_mad_u64_u32 v[44:45], s[36:37], v69, s31, v[10:11]
	v_mad_u64_u32 v[46:47], s[36:37], v72, s31, v[10:11]
	v_mad_u64_u32 v[48:49], s[36:37], v71, s31, v[10:11]
	v_mad_u64_u32 v[50:51], s[36:37], v74, s31, v[10:11]
	v_mad_u64_u32 v[52:53], s[36:37], v73, s31, v[10:11]
	v_mad_u64_u32 v[54:55], s[36:37], v76, s31, v[10:11]
	v_mad_u64_u32 v[56:57], s[36:37], v75, s31, v[10:11]
	v_mad_u64_u32 v[58:59], s[36:37], v78, s31, v[10:11]
	v_mad_u64_u32 v[60:61], s[36:37], v77, s31, v[10:11]
	v_mad_u64_u32 v[62:63], s[36:37], v80, s31, v[10:11]
	v_mad_u64_u32 v[64:65], s[36:37], v79, s31, v[10:11]
	s_lshl_b32 s36, s33, 1
	s_lshl_b32 s37, s34, 1
	v_or_b32_e32 v112, s36, v1
	v_or_b32_e32 v144, s37, v6
	s_add_i32 s38, s36, 4
	s_add_i32 s39, s37, 4
	s_add_i32 s40, s36, 8
	s_add_i32 s41, s37, 8
	s_add_i32 s42, s36, 12
	s_add_i32 s43, s37, 12
	s_add_i32 s44, s36, 16
	s_add_i32 s45, s37, 16
	s_add_i32 s46, s36, 20
	s_add_i32 s47, s37, 20
	s_add_i32 s48, s36, 24
	s_add_i32 s49, s37, 24
	s_add_i32 s36, s36, 28
	s_add_i32 s37, s37, 28
	v_add_u32_e32 v114, s16, v144
	v_or_b32_e32 v145, s38, v1
	v_or_b32_e32 v146, s39, v6
	v_or_b32_e32 v147, s40, v1
	v_or_b32_e32 v148, s41, v6
	v_or_b32_e32 v149, s42, v1
	v_or_b32_e32 v150, s43, v6
	v_or_b32_e32 v151, s44, v1
	v_or_b32_e32 v152, s45, v6
	v_or_b32_e32 v153, s46, v1
	v_or_b32_e32 v154, s47, v6
	v_or_b32_e32 v155, s48, v1
	v_or_b32_e32 v156, s49, v6
	v_or_b32_e32 v157, s36, v1
	v_or_b32_e32 v158, s37, v6
	v_add_u32_e32 v110, s23, v112
	v_ashrrev_i32_e32 v115, 31, v114
	v_add_u32_e32 v116, s23, v145
	v_add_u32_e32 v118, s16, v146
	v_add_u32_e32 v120, s23, v147
	v_add_u32_e32 v122, s16, v148
	v_add_u32_e32 v124, s23, v149
	v_add_u32_e32 v126, s16, v150
	v_add_u32_e32 v128, s23, v151
	v_add_u32_e32 v130, s16, v152
	v_add_u32_e32 v132, s23, v153
	v_add_u32_e32 v134, s16, v154
	v_add_u32_e32 v136, s23, v155
	v_add_u32_e32 v138, s16, v156
	v_add_u32_e32 v140, s23, v157
	v_add_u32_e32 v142, s16, v158
	v_ashrrev_i32_e32 v111, 31, v110
	v_lshlrev_b64 v[114:115], 12, v[114:115]
	v_ashrrev_i32_e32 v119, 31, v118
	v_ashrrev_i32_e32 v117, 31, v116
	v_ashrrev_i32_e32 v123, 31, v122
	v_ashrrev_i32_e32 v121, 31, v120
	v_ashrrev_i32_e32 v127, 31, v126
	v_ashrrev_i32_e32 v125, 31, v124
	v_ashrrev_i32_e32 v131, 31, v130
	v_ashrrev_i32_e32 v129, 31, v128
	v_ashrrev_i32_e32 v135, 31, v134
	v_ashrrev_i32_e32 v133, 31, v132
	v_ashrrev_i32_e32 v139, 31, v138
	v_ashrrev_i32_e32 v137, 31, v136
	v_ashrrev_i32_e32 v143, 31, v142
	v_ashrrev_i32_e32 v141, 31, v140
	v_lshlrev_b64 v[110:111], 12, v[110:111]
	v_lshl_add_u64 v[114:115], v[2:3], 0, v[114:115]
	v_lshlrev_b64 v[116:117], 12, v[116:117]
	v_lshlrev_b64 v[118:119], 12, v[118:119]
	v_lshlrev_b64 v[120:121], 12, v[120:121]
	v_lshlrev_b64 v[122:123], 12, v[122:123]
	v_lshlrev_b64 v[124:125], 12, v[124:125]
	v_lshlrev_b64 v[126:127], 12, v[126:127]
	v_lshlrev_b64 v[128:129], 12, v[128:129]
	v_lshlrev_b64 v[130:131], 12, v[130:131]
	v_lshlrev_b64 v[132:133], 12, v[132:133]
	v_lshlrev_b64 v[134:135], 12, v[134:135]
	v_lshlrev_b64 v[136:137], 12, v[136:137]
	v_lshlrev_b64 v[138:139], 12, v[138:139]
	v_lshlrev_b64 v[140:141], 12, v[140:141]
	v_lshlrev_b64 v[142:143], 12, v[142:143]
	v_lshl_add_u64 v[110:111], v[2:3], 0, v[110:111]
	v_lshl_add_u64 v[118:119], v[2:3], 0, v[118:119]
	v_lshl_add_u64 v[116:117], v[2:3], 0, v[116:117]
	v_lshl_add_u64 v[122:123], v[2:3], 0, v[122:123]
	v_lshl_add_u64 v[120:121], v[2:3], 0, v[120:121]
	v_lshl_add_u64 v[126:127], v[2:3], 0, v[126:127]
	v_lshl_add_u64 v[124:125], v[2:3], 0, v[124:125]
	v_lshl_add_u64 v[130:131], v[2:3], 0, v[130:131]
	v_lshl_add_u64 v[128:129], v[2:3], 0, v[128:129]
	v_lshl_add_u64 v[134:135], v[2:3], 0, v[134:135]
	v_lshl_add_u64 v[132:133], v[2:3], 0, v[132:133]
	v_lshl_add_u64 v[138:139], v[2:3], 0, v[138:139]
	v_lshl_add_u64 v[136:137], v[2:3], 0, v[136:137]
	v_lshl_add_u64 v[142:143], v[2:3], 0, v[142:143]
	v_lshl_add_u64 v[140:141], v[2:3], 0, v[140:141]
	global_load_dword v159, v[114:115], off nt
	global_load_dword v160, v[110:111], off nt
	global_load_dword v161, v[118:119], off nt
	global_load_dword v162, v[116:117], off nt
	global_load_dword v163, v[122:123], off nt
	global_load_dword v164, v[120:121], off nt
	global_load_dword v165, v[126:127], off nt
	global_load_dword v166, v[124:125], off nt
	global_load_dword v167, v[130:131], off nt
	global_load_dword v168, v[128:129], off nt
	global_load_dword v169, v[134:135], off nt
	global_load_dword v170, v[132:133], off nt
	global_load_dword v171, v[138:139], off nt
	global_load_dword v172, v[136:137], off nt
	global_load_dword v173, v[142:143], off nt
	global_load_dword v174, v[140:141], off nt
	s_add_i32 s34, s34, 16
	s_add_i32 s33, s33, 16
	s_add_i32 s35, s35, -16
	v_mad_u64_u32 v[110:111], s[36:37], v144, s31, v[10:11]
	s_cmp_lg_u32 s35, 0
	v_mad_u64_u32 v[114:115], s[36:37], v112, s31, v[10:11]
	v_mad_u64_u32 v[116:117], s[36:37], v146, s31, v[10:11]
	v_mad_u64_u32 v[118:119], s[36:37], v145, s31, v[10:11]
	v_mad_u64_u32 v[120:121], s[36:37], v148, s31, v[10:11]
	v_mad_u64_u32 v[122:123], s[36:37], v147, s31, v[10:11]
	v_mad_u64_u32 v[124:125], s[36:37], v150, s31, v[10:11]
	v_mad_u64_u32 v[126:127], s[36:37], v149, s31, v[10:11]
	v_mad_u64_u32 v[128:129], s[36:37], v152, s31, v[10:11]
	v_mad_u64_u32 v[130:131], s[36:37], v151, s31, v[10:11]
	v_mad_u64_u32 v[132:133], s[36:37], v154, s31, v[10:11]
	v_mad_u64_u32 v[134:135], s[36:37], v153, s31, v[10:11]
	v_mad_u64_u32 v[136:137], s[36:37], v156, s31, v[10:11]
	v_mad_u64_u32 v[138:139], s[36:37], v155, s31, v[10:11]
	v_mad_u64_u32 v[140:141], s[36:37], v158, s31, v[10:11]
	v_mad_u64_u32 v[142:143], s[36:37], v157, s31, v[10:11]
	s_waitcnt vmcnt(31)
	ds_write_b32 v4, v81
	s_waitcnt vmcnt(30)
	ds_write_b32 v32, v82
	s_waitcnt vmcnt(29)
	ds_write_b32 v34, v83
	s_waitcnt vmcnt(28)
	ds_write_b32 v40, v84
	s_waitcnt vmcnt(27)
	ds_write_b32 v42, v85
	s_waitcnt vmcnt(26)
	ds_write_b32 v44, v86
	s_waitcnt vmcnt(25)
	ds_write_b32 v46, v87
	s_waitcnt vmcnt(24)
	ds_write_b32 v48, v88
	s_waitcnt vmcnt(23)
	ds_write_b32 v50, v89
	s_waitcnt vmcnt(22)
	ds_write_b32 v52, v90
	s_waitcnt vmcnt(21)
	ds_write_b32 v54, v91
	s_waitcnt vmcnt(20)
	ds_write_b32 v56, v92
	s_waitcnt vmcnt(19)
	ds_write_b32 v58, v93
	s_waitcnt vmcnt(18)
	ds_write_b32 v60, v94
	s_waitcnt vmcnt(17)
	ds_write_b32 v62, v95
	s_waitcnt vmcnt(16)
	ds_write_b32 v64, v96
	s_waitcnt vmcnt(15)
	ds_write_b32 v110, v159
	s_waitcnt vmcnt(14)
	ds_write_b32 v114, v160
	s_waitcnt vmcnt(13)
	ds_write_b32 v116, v161
	s_waitcnt vmcnt(12)
	ds_write_b32 v118, v162
	s_waitcnt vmcnt(11)
	ds_write_b32 v120, v163
	s_waitcnt vmcnt(10)
	ds_write_b32 v122, v164
	s_waitcnt vmcnt(9)
	ds_write_b32 v124, v165
	s_waitcnt vmcnt(8)
	ds_write_b32 v126, v166
	s_waitcnt vmcnt(7)
	ds_write_b32 v128, v167
	s_waitcnt vmcnt(6)
	ds_write_b32 v130, v168
	s_waitcnt vmcnt(5)
	ds_write_b32 v132, v169
	s_waitcnt vmcnt(4)
	ds_write_b32 v134, v170
	s_waitcnt vmcnt(3)
	ds_write_b32 v136, v171
	s_waitcnt vmcnt(2)
	ds_write_b32 v138, v172
	s_waitcnt vmcnt(1)
	ds_write_b32 v140, v173
	s_waitcnt vmcnt(0)
	ds_write_b32 v142, v174

.LBB0_387:
	s_lshl_b32 s47, s25, 1
	s_lshl_b32 s48, s20, 1
	v_or_b32_e32 v11, s47, v1
	v_or_b32_e32 v29, s48, v8
	s_add_i32 s49, s47, 4
	s_add_i32 s50, s48, 4
	s_add_i32 s51, s47, 8
	s_add_i32 s52, s48, 8
	s_add_i32 s53, s47, 12
	s_add_i32 s54, s48, 12
	s_add_i32 s55, s47, 16
	s_add_i32 s60, s48, 16
	s_add_i32 s61, s47, 20
	s_add_i32 s62, s48, 20
	s_add_i32 s63, s47, 24
	s_add_i32 s64, s48, 24
	s_add_i32 s47, s47, 28
	s_add_i32 s48, s48, 28
	v_add_u32_e32 v6, s26, v29
	v_or_b32_e32 v60, s49, v1
	v_or_b32_e32 v61, s50, v8
	v_or_b32_e32 v62, s51, v1
	v_or_b32_e32 v63, s52, v8
	v_or_b32_e32 v64, s53, v1
	v_or_b32_e32 v65, s54, v8
	v_or_b32_e32 v66, s55, v1
	v_or_b32_e32 v67, s60, v8
	v_or_b32_e32 v68, s61, v1
	v_or_b32_e32 v69, s62, v8
	v_or_b32_e32 v70, s63, v1
	v_or_b32_e32 v71, s64, v8
	v_or_b32_e32 v72, s47, v1
	v_or_b32_e32 v73, s48, v8
	v_add_u32_e32 v30, s21, v11
	v_mad_i64_i32 v[6:7], s[48:49], v6, s31, v[4:5]
	v_add_u32_e32 v34, s21, v60
	v_add_u32_e32 v32, s26, v61
	v_add_u32_e32 v38, s21, v62
	v_add_u32_e32 v36, s26, v63
	v_add_u32_e32 v42, s21, v64
	v_add_u32_e32 v40, s26, v65
	v_add_u32_e32 v46, s21, v66
	v_add_u32_e32 v44, s26, v67
	v_add_u32_e32 v50, s21, v68
	v_add_u32_e32 v48, s26, v69
	v_add_u32_e32 v54, s21, v70
	v_add_u32_e32 v52, s26, v71
	v_add_u32_e32 v58, s21, v72
	v_add_u32_e32 v56, s26, v73
	v_mad_i64_i32 v[30:31], s[48:49], v30, s31, v[4:5]
	v_mad_i64_i32 v[32:33], s[48:49], v32, s31, v[4:5]
	v_mad_i64_i32 v[34:35], s[48:49], v34, s31, v[4:5]
	v_mad_i64_i32 v[36:37], s[48:49], v36, s31, v[4:5]
	v_mad_i64_i32 v[38:39], s[48:49], v38, s31, v[4:5]
	v_mad_i64_i32 v[40:41], s[48:49], v40, s31, v[4:5]
	v_mad_i64_i32 v[42:43], s[48:49], v42, s31, v[4:5]
	v_mad_i64_i32 v[44:45], s[48:49], v44, s31, v[4:5]
	v_mad_i64_i32 v[46:47], s[48:49], v46, s31, v[4:5]
	v_mad_i64_i32 v[48:49], s[48:49], v48, s31, v[4:5]
	v_mad_i64_i32 v[50:51], s[48:49], v50, s31, v[4:5]
	v_mad_i64_i32 v[52:53], s[48:49], v52, s31, v[4:5]
	v_mad_i64_i32 v[54:55], s[48:49], v54, s31, v[4:5]
	v_mad_i64_i32 v[56:57], s[48:49], v56, s31, v[4:5]
	v_mad_i64_i32 v[58:59], s[48:49], v58, s31, v[4:5]
	global_load_dword v74, v[6:7], off nt
	global_load_dword v75, v[30:31], off nt
	global_load_dword v76, v[32:33], off nt
	global_load_dword v77, v[34:35], off nt
	global_load_dword v78, v[36:37], off nt
	global_load_dword v79, v[38:39], off nt
	global_load_dword v80, v[40:41], off nt
	global_load_dword v81, v[42:43], off nt
	global_load_dword v82, v[44:45], off nt
	global_load_dword v83, v[46:47], off nt
	global_load_dword v84, v[48:49], off nt
	global_load_dword v85, v[50:51], off nt
	global_load_dword v86, v[52:53], off nt
	global_load_dword v87, v[54:55], off nt
	global_load_dword v88, v[56:57], off nt
	global_load_dword v89, v[58:59], off nt
	s_add_i32 s20, s20, 16
	s_add_i32 s25, s25, 16
	s_add_i32 s27, s27, -16
	v_mad_u64_u32 v[6:7], s[48:49], v29, s33, v[10:11]
	s_cmp_lg_u32 s27, 0
	v_mad_u64_u32 v[30:31], s[48:49], v11, s33, v[10:11]
	v_mad_u64_u32 v[32:33], s[48:49], v61, s33, v[10:11]
	v_mad_u64_u32 v[34:35], s[48:49], v60, s33, v[10:11]
	v_mad_u64_u32 v[36:37], s[48:49], v63, s33, v[10:11]
	v_mad_u64_u32 v[38:39], s[48:49], v62, s33, v[10:11]
	v_mad_u64_u32 v[40:41], s[48:49], v65, s33, v[10:11]
	v_mad_u64_u32 v[42:43], s[48:49], v64, s33, v[10:11]
	v_mad_u64_u32 v[44:45], s[48:49], v67, s33, v[10:11]
	v_mad_u64_u32 v[46:47], s[48:49], v66, s33, v[10:11]
	v_mad_u64_u32 v[48:49], s[48:49], v69, s33, v[10:11]
	v_mad_u64_u32 v[50:51], s[48:49], v68, s33, v[10:11]
	v_mad_u64_u32 v[52:53], s[48:49], v71, s33, v[10:11]
	v_mad_u64_u32 v[54:55], s[48:49], v70, s33, v[10:11]
	v_mad_u64_u32 v[56:57], s[48:49], v73, s33, v[10:11]
	v_mad_u64_u32 v[58:59], s[48:49], v72, s33, v[10:11]
	s_lshl_b32 s47, s25, 1
	s_lshl_b32 s48, s20, 1
	v_or_b32_e32 v112, s47, v1
	v_or_b32_e32 v113, s48, v8
	s_add_i32 s49, s47, 4
	s_add_i32 s50, s48, 4
	s_add_i32 s51, s47, 8
	s_add_i32 s52, s48, 8
	s_add_i32 s53, s47, 12
	s_add_i32 s54, s48, 12
	s_add_i32 s55, s47, 16
	s_add_i32 s60, s48, 16
	s_add_i32 s61, s47, 20
	s_add_i32 s62, s48, 20
	s_add_i32 s63, s47, 24
	s_add_i32 s64, s48, 24
	s_add_i32 s47, s47, 28
	s_add_i32 s48, s48, 28
	v_add_u32_e32 v110, s26, v113
	v_or_b32_e32 v144, s49, v1
	v_or_b32_e32 v145, s50, v8
	v_or_b32_e32 v146, s51, v1
	v_or_b32_e32 v147, s52, v8
	v_or_b32_e32 v148, s53, v1
	v_or_b32_e32 v149, s54, v8
	v_or_b32_e32 v150, s55, v1
	v_or_b32_e32 v151, s60, v8
	v_or_b32_e32 v152, s61, v1
	v_or_b32_e32 v153, s62, v8
	v_or_b32_e32 v154, s63, v1
	v_or_b32_e32 v155, s64, v8
	v_or_b32_e32 v156, s47, v1
	v_or_b32_e32 v157, s48, v8
	v_add_u32_e32 v114, s21, v112
	v_mad_i64_i32 v[110:111], s[48:49], v110, s31, v[4:5]
	v_add_u32_e32 v118, s21, v144
	v_add_u32_e32 v116, s26, v145
	v_add_u32_e32 v122, s21, v146
	v_add_u32_e32 v120, s26, v147
	v_add_u32_e32 v126, s21, v148
	v_add_u32_e32 v124, s26, v149
	v_add_u32_e32 v130, s21, v150
	v_add_u32_e32 v128, s26, v151
	v_add_u32_e32 v134, s21, v152
	v_add_u32_e32 v132, s26, v153
	v_add_u32_e32 v138, s21, v154
	v_add_u32_e32 v136, s26, v155
	v_add_u32_e32 v142, s21, v156
	v_add_u32_e32 v140, s26, v157
	v_mad_i64_i32 v[114:115], s[48:49], v114, s31, v[4:5]
	v_mad_i64_i32 v[116:117], s[48:49], v116, s31, v[4:5]
	v_mad_i64_i32 v[118:119], s[48:49], v118, s31, v[4:5]
	v_mad_i64_i32 v[120:121], s[48:49], v120, s31, v[4:5]
	v_mad_i64_i32 v[122:123], s[48:49], v122, s31, v[4:5]
	v_mad_i64_i32 v[124:125], s[48:49], v124, s31, v[4:5]
	v_mad_i64_i32 v[126:127], s[48:49], v126, s31, v[4:5]
	v_mad_i64_i32 v[128:129], s[48:49], v128, s31, v[4:5]
	v_mad_i64_i32 v[130:131], s[48:49], v130, s31, v[4:5]
	v_mad_i64_i32 v[132:133], s[48:49], v132, s31, v[4:5]
	v_mad_i64_i32 v[134:135], s[48:49], v134, s31, v[4:5]
	v_mad_i64_i32 v[136:137], s[48:49], v136, s31, v[4:5]
	v_mad_i64_i32 v[138:139], s[48:49], v138, s31, v[4:5]
	v_mad_i64_i32 v[140:141], s[48:49], v140, s31, v[4:5]
	v_mad_i64_i32 v[142:143], s[48:49], v142, s31, v[4:5]
	global_load_dword v158, v[110:111], off nt
	global_load_dword v159, v[114:115], off nt
	global_load_dword v160, v[116:117], off nt
	global_load_dword v161, v[118:119], off nt
	global_load_dword v162, v[120:121], off nt
	global_load_dword v163, v[122:123], off nt
	global_load_dword v164, v[124:125], off nt
	global_load_dword v165, v[126:127], off nt
	global_load_dword v166, v[128:129], off nt
	global_load_dword v167, v[130:131], off nt
	global_load_dword v168, v[132:133], off nt
	global_load_dword v169, v[134:135], off nt
	global_load_dword v170, v[136:137], off nt
	global_load_dword v171, v[138:139], off nt
	global_load_dword v172, v[140:141], off nt
	global_load_dword v173, v[142:143], off nt
	s_add_i32 s20, s20, 16
	s_add_i32 s25, s25, 16
	s_add_i32 s27, s27, -16
	v_mad_u64_u32 v[110:111], s[48:49], v113, s33, v[10:11]
	s_cmp_lg_u32 s27, 0
	v_mad_u64_u32 v[114:115], s[48:49], v112, s33, v[10:11]
	v_mad_u64_u32 v[116:117], s[48:49], v145, s33, v[10:11]
	v_mad_u64_u32 v[118:119], s[48:49], v144, s33, v[10:11]
	v_mad_u64_u32 v[120:121], s[48:49], v147, s33, v[10:11]
	v_mad_u64_u32 v[122:123], s[48:49], v146, s33, v[10:11]
	v_mad_u64_u32 v[124:125], s[48:49], v149, s33, v[10:11]
	v_mad_u64_u32 v[126:127], s[48:49], v148, s33, v[10:11]
	v_mad_u64_u32 v[128:129], s[48:49], v151, s33, v[10:11]
	v_mad_u64_u32 v[130:131], s[48:49], v150, s33, v[10:11]
	v_mad_u64_u32 v[132:133], s[48:49], v153, s33, v[10:11]
	v_mad_u64_u32 v[134:135], s[48:49], v152, s33, v[10:11]
	v_mad_u64_u32 v[136:137], s[48:49], v155, s33, v[10:11]
	v_mad_u64_u32 v[138:139], s[48:49], v154, s33, v[10:11]
	v_mad_u64_u32 v[140:141], s[48:49], v157, s33, v[10:11]
	v_mad_u64_u32 v[142:143], s[48:49], v156, s33, v[10:11]
	s_waitcnt vmcnt(16)
	ds_write_b32 v6, v74
	s_waitcnt vmcnt(30)
	ds_write_b32 v30, v75
	s_waitcnt vmcnt(29)
	ds_write_b32 v32, v76
	s_waitcnt vmcnt(28)
	ds_write_b32 v34, v77
	s_waitcnt vmcnt(27)
	ds_write_b32 v36, v78
	s_waitcnt vmcnt(26)
	ds_write_b32 v38, v79
	s_waitcnt vmcnt(25)
	ds_write_b32 v40, v80
	s_waitcnt vmcnt(24)
	ds_write_b32 v42, v81
	s_waitcnt vmcnt(23)
	ds_write_b32 v44, v82
	s_waitcnt vmcnt(22)
	ds_write_b32 v46, v83
	s_waitcnt vmcnt(21)
	ds_write_b32 v48, v84
	s_waitcnt vmcnt(20)
	ds_write_b32 v50, v85
	s_waitcnt vmcnt(19)
	ds_write_b32 v52, v86
	s_waitcnt vmcnt(18)
	ds_write_b32 v54, v87
	s_waitcnt vmcnt(17)
	ds_write_b32 v56, v88
	s_waitcnt vmcnt(16)
	ds_write_b32 v58, v89
	s_waitcnt vmcnt(0)
	ds_write_b32 v110, v158
	s_waitcnt vmcnt(14)
	ds_write_b32 v114, v159
	s_waitcnt vmcnt(13)
	ds_write_b32 v116, v160
	s_waitcnt vmcnt(12)
	ds_write_b32 v118, v161
	s_waitcnt vmcnt(11)
	ds_write_b32 v120, v162
	s_waitcnt vmcnt(10)
	ds_write_b32 v122, v163
	s_waitcnt vmcnt(9)
	ds_write_b32 v124, v164
	s_waitcnt vmcnt(8)
	ds_write_b32 v126, v165
	s_waitcnt vmcnt(7)
	ds_write_b32 v128, v166
	s_waitcnt vmcnt(6)
	ds_write_b32 v130, v167
	s_waitcnt vmcnt(5)
	ds_write_b32 v132, v168
	s_waitcnt vmcnt(4)
	ds_write_b32 v134, v169
	s_waitcnt vmcnt(3)
	ds_write_b32 v136, v170
	s_waitcnt vmcnt(2)
	ds_write_b32 v138, v171
	s_waitcnt vmcnt(1)
	ds_write_b32 v140, v172
	s_waitcnt vmcnt(0)
	ds_write_b32 v142, v173

.LBB0_401:
	s_lshl_b32 s42, s23, 1
	s_lshl_b32 s43, s27, 1
	v_or_b32_e32 v11, s42, v1
	v_or_b32_e32 v29, s43, v8
	s_add_i32 s44, s42, 4
	s_add_i32 s45, s43, 4
	s_add_i32 s46, s42, 8
	s_add_i32 s47, s43, 8
	s_add_i32 s48, s42, 12
	s_add_i32 s49, s43, 12
	s_add_i32 s50, s42, 16
	s_add_i32 s51, s43, 16
	s_add_i32 s52, s42, 20
	s_add_i32 s53, s43, 20
	s_add_i32 s54, s42, 24
	s_add_i32 s55, s43, 24
	s_add_i32 s42, s42, 28
	s_add_i32 s43, s43, 28
	v_add_u32_e32 v32, s22, v29
	v_or_b32_e32 v62, s44, v1
	v_or_b32_e32 v63, s45, v8
	v_or_b32_e32 v64, s46, v1
	v_or_b32_e32 v65, s47, v8
	v_or_b32_e32 v66, s48, v1
	v_or_b32_e32 v67, s49, v8
	v_or_b32_e32 v68, s50, v1
	v_or_b32_e32 v69, s51, v8
	v_or_b32_e32 v70, s52, v1
	v_or_b32_e32 v71, s53, v8
	v_or_b32_e32 v72, s54, v1
	v_or_b32_e32 v73, s55, v8
	v_or_b32_e32 v74, s42, v1
	v_or_b32_e32 v75, s43, v8
	v_add_u32_e32 v6, s21, v11
	v_ashrrev_i32_e32 v33, 31, v32
	v_add_u32_e32 v34, s21, v62
	v_add_u32_e32 v36, s22, v63
	v_add_u32_e32 v38, s21, v64
	v_add_u32_e32 v40, s22, v65
	v_add_u32_e32 v42, s21, v66
	v_add_u32_e32 v44, s22, v67
	v_add_u32_e32 v46, s21, v68
	v_add_u32_e32 v48, s22, v69
	v_add_u32_e32 v50, s21, v70
	v_add_u32_e32 v52, s22, v71
	v_add_u32_e32 v54, s21, v72
	v_add_u32_e32 v56, s22, v73
	v_add_u32_e32 v58, s21, v74
	v_add_u32_e32 v60, s22, v75
	v_ashrrev_i32_e32 v7, 31, v6
	v_lshlrev_b64 v[32:33], 12, v[32:33]
	v_ashrrev_i32_e32 v37, 31, v36
	v_ashrrev_i32_e32 v35, 31, v34
	v_ashrrev_i32_e32 v41, 31, v40
	v_ashrrev_i32_e32 v39, 31, v38
	v_ashrrev_i32_e32 v45, 31, v44
	v_ashrrev_i32_e32 v43, 31, v42
	v_ashrrev_i32_e32 v49, 31, v48
	v_ashrrev_i32_e32 v47, 31, v46
	v_ashrrev_i32_e32 v53, 31, v52
	v_ashrrev_i32_e32 v51, 31, v50
	v_ashrrev_i32_e32 v57, 31, v56
	v_ashrrev_i32_e32 v55, 31, v54
	v_ashrrev_i32_e32 v61, 31, v60
	v_ashrrev_i32_e32 v59, 31, v58
	v_lshlrev_b64 v[6:7], 12, v[6:7]
	v_lshl_add_u64 v[32:33], v[4:5], 0, v[32:33]
	v_lshlrev_b64 v[34:35], 12, v[34:35]
	v_lshlrev_b64 v[36:37], 12, v[36:37]
	v_lshlrev_b64 v[38:39], 12, v[38:39]
	v_lshlrev_b64 v[40:41], 12, v[40:41]
	v_lshlrev_b64 v[42:43], 12, v[42:43]
	v_lshlrev_b64 v[44:45], 12, v[44:45]
	v_lshlrev_b64 v[46:47], 12, v[46:47]
	v_lshlrev_b64 v[48:49], 12, v[48:49]
	v_lshlrev_b64 v[50:51], 12, v[50:51]
	v_lshlrev_b64 v[52:53], 12, v[52:53]
	v_lshlrev_b64 v[54:55], 12, v[54:55]
	v_lshlrev_b64 v[56:57], 12, v[56:57]
	v_lshlrev_b64 v[58:59], 12, v[58:59]
	v_lshlrev_b64 v[60:61], 12, v[60:61]
	v_lshl_add_u64 v[6:7], v[4:5], 0, v[6:7]
	v_lshl_add_u64 v[36:37], v[4:5], 0, v[36:37]
	v_lshl_add_u64 v[34:35], v[4:5], 0, v[34:35]
	v_lshl_add_u64 v[40:41], v[4:5], 0, v[40:41]
	v_lshl_add_u64 v[38:39], v[4:5], 0, v[38:39]
	v_lshl_add_u64 v[44:45], v[4:5], 0, v[44:45]
	v_lshl_add_u64 v[42:43], v[4:5], 0, v[42:43]
	v_lshl_add_u64 v[48:49], v[4:5], 0, v[48:49]
	v_lshl_add_u64 v[46:47], v[4:5], 0, v[46:47]
	v_lshl_add_u64 v[52:53], v[4:5], 0, v[52:53]
	v_lshl_add_u64 v[50:51], v[4:5], 0, v[50:51]
	v_lshl_add_u64 v[56:57], v[4:5], 0, v[56:57]
	v_lshl_add_u64 v[54:55], v[4:5], 0, v[54:55]
	v_lshl_add_u64 v[60:61], v[4:5], 0, v[60:61]
	v_lshl_add_u64 v[58:59], v[4:5], 0, v[58:59]
	global_load_dword v76, v[32:33], off nt
	global_load_dword v77, v[6:7], off nt
	global_load_dword v78, v[36:37], off nt
	global_load_dword v79, v[34:35], off nt
	global_load_dword v80, v[40:41], off nt
	global_load_dword v81, v[38:39], off nt
	global_load_dword v82, v[44:45], off nt
	global_load_dword v83, v[42:43], off nt
	global_load_dword v84, v[48:49], off nt
	global_load_dword v85, v[46:47], off nt
	global_load_dword v86, v[52:53], off nt
	global_load_dword v87, v[50:51], off nt
	global_load_dword v88, v[56:57], off nt
	global_load_dword v89, v[54:55], off nt
	global_load_dword v90, v[60:61], off nt
	global_load_dword v91, v[58:59], off nt
	s_add_i32 s27, s27, 16
	s_add_i32 s23, s23, 16
	s_add_i32 s41, s41, -16
	v_mad_u64_u32 v[6:7], s[42:43], v29, s33, v[10:11]
	s_cmp_lg_u32 s41, 0
	v_mad_u64_u32 v[32:33], s[42:43], v11, s33, v[10:11]
	v_mad_u64_u32 v[34:35], s[42:43], v63, s33, v[10:11]
	v_mad_u64_u32 v[36:37], s[42:43], v62, s33, v[10:11]
	v_mad_u64_u32 v[38:39], s[42:43], v65, s33, v[10:11]
	v_mad_u64_u32 v[40:41], s[42:43], v64, s33, v[10:11]
	v_mad_u64_u32 v[42:43], s[42:43], v67, s33, v[10:11]
	v_mad_u64_u32 v[44:45], s[42:43], v66, s33, v[10:11]
	v_mad_u64_u32 v[46:47], s[42:43], v69, s33, v[10:11]
	v_mad_u64_u32 v[48:49], s[42:43], v68, s33, v[10:11]
	v_mad_u64_u32 v[50:51], s[42:43], v71, s33, v[10:11]
	v_mad_u64_u32 v[52:53], s[42:43], v70, s33, v[10:11]
	v_mad_u64_u32 v[54:55], s[42:43], v73, s33, v[10:11]
	v_mad_u64_u32 v[56:57], s[42:43], v72, s33, v[10:11]
	v_mad_u64_u32 v[58:59], s[42:43], v75, s33, v[10:11]
	v_mad_u64_u32 v[60:61], s[42:43], v74, s33, v[10:11]
	s_lshl_b32 s42, s23, 1
	s_lshl_b32 s43, s27, 1
	v_or_b32_e32 v112, s42, v1
	v_or_b32_e32 v113, s43, v8
	s_add_i32 s44, s42, 4
	s_add_i32 s45, s43, 4
	s_add_i32 s46, s42, 8
	s_add_i32 s47, s43, 8
	s_add_i32 s48, s42, 12
	s_add_i32 s49, s43, 12
	s_add_i32 s50, s42, 16
	s_add_i32 s51, s43, 16
	s_add_i32 s52, s42, 20
	s_add_i32 s53, s43, 20
	s_add_i32 s54, s42, 24
	s_add_i32 s55, s43, 24
	s_add_i32 s42, s42, 28
	s_add_i32 s43, s43, 28
	v_add_u32_e32 v114, s22, v113
	v_or_b32_e32 v144, s44, v1
	v_or_b32_e32 v145, s45, v8
	v_or_b32_e32 v146, s46, v1
	v_or_b32_e32 v147, s47, v8
	v_or_b32_e32 v148, s48, v1
	v_or_b32_e32 v149, s49, v8
	v_or_b32_e32 v150, s50, v1
	v_or_b32_e32 v151, s51, v8
	v_or_b32_e32 v152, s52, v1
	v_or_b32_e32 v153, s53, v8
	v_or_b32_e32 v154, s54, v1
	v_or_b32_e32 v155, s55, v8
	v_or_b32_e32 v156, s42, v1
	v_or_b32_e32 v157, s43, v8
	v_add_u32_e32 v110, s21, v112
	v_ashrrev_i32_e32 v115, 31, v114
	v_add_u32_e32 v116, s21, v144
	v_add_u32_e32 v118, s22, v145
	v_add_u32_e32 v120, s21, v146
	v_add_u32_e32 v122, s22, v147
	v_add_u32_e32 v124, s21, v148
	v_add_u32_e32 v126, s22, v149
	v_add_u32_e32 v128, s21, v150
	v_add_u32_e32 v130, s22, v151
	v_add_u32_e32 v132, s21, v152
	v_add_u32_e32 v134, s22, v153
	v_add_u32_e32 v136, s21, v154
	v_add_u32_e32 v138, s22, v155
	v_add_u32_e32 v140, s21, v156
	v_add_u32_e32 v142, s22, v157
	v_ashrrev_i32_e32 v111, 31, v110
	v_lshlrev_b64 v[114:115], 12, v[114:115]
	v_ashrrev_i32_e32 v119, 31, v118
	v_ashrrev_i32_e32 v117, 31, v116
	v_ashrrev_i32_e32 v123, 31, v122
	v_ashrrev_i32_e32 v121, 31, v120
	v_ashrrev_i32_e32 v127, 31, v126
	v_ashrrev_i32_e32 v125, 31, v124
	v_ashrrev_i32_e32 v131, 31, v130
	v_ashrrev_i32_e32 v129, 31, v128
	v_ashrrev_i32_e32 v135, 31, v134
	v_ashrrev_i32_e32 v133, 31, v132
	v_ashrrev_i32_e32 v139, 31, v138
	v_ashrrev_i32_e32 v137, 31, v136
	v_ashrrev_i32_e32 v143, 31, v142
	v_ashrrev_i32_e32 v141, 31, v140
	v_lshlrev_b64 v[110:111], 12, v[110:111]
	v_lshl_add_u64 v[114:115], v[4:5], 0, v[114:115]
	v_lshlrev_b64 v[116:117], 12, v[116:117]
	v_lshlrev_b64 v[118:119], 12, v[118:119]
	v_lshlrev_b64 v[120:121], 12, v[120:121]
	v_lshlrev_b64 v[122:123], 12, v[122:123]
	v_lshlrev_b64 v[124:125], 12, v[124:125]
	v_lshlrev_b64 v[126:127], 12, v[126:127]
	v_lshlrev_b64 v[128:129], 12, v[128:129]
	v_lshlrev_b64 v[130:131], 12, v[130:131]
	v_lshlrev_b64 v[132:133], 12, v[132:133]
	v_lshlrev_b64 v[134:135], 12, v[134:135]
	v_lshlrev_b64 v[136:137], 12, v[136:137]
	v_lshlrev_b64 v[138:139], 12, v[138:139]
	v_lshlrev_b64 v[140:141], 12, v[140:141]
	v_lshlrev_b64 v[142:143], 12, v[142:143]
	v_lshl_add_u64 v[110:111], v[4:5], 0, v[110:111]
	v_lshl_add_u64 v[118:119], v[4:5], 0, v[118:119]
	v_lshl_add_u64 v[116:117], v[4:5], 0, v[116:117]
	v_lshl_add_u64 v[122:123], v[4:5], 0, v[122:123]
	v_lshl_add_u64 v[120:121], v[4:5], 0, v[120:121]
	v_lshl_add_u64 v[126:127], v[4:5], 0, v[126:127]
	v_lshl_add_u64 v[124:125], v[4:5], 0, v[124:125]
	v_lshl_add_u64 v[130:131], v[4:5], 0, v[130:131]
	v_lshl_add_u64 v[128:129], v[4:5], 0, v[128:129]
	v_lshl_add_u64 v[134:135], v[4:5], 0, v[134:135]
	v_lshl_add_u64 v[132:133], v[4:5], 0, v[132:133]
	v_lshl_add_u64 v[138:139], v[4:5], 0, v[138:139]
	v_lshl_add_u64 v[136:137], v[4:5], 0, v[136:137]
	v_lshl_add_u64 v[142:143], v[4:5], 0, v[142:143]
	v_lshl_add_u64 v[140:141], v[4:5], 0, v[140:141]
	global_load_dword v158, v[114:115], off
	global_load_dword v159, v[110:111], off
	global_load_dword v160, v[118:119], off
	global_load_dword v161, v[116:117], off
	global_load_dword v162, v[122:123], off
	global_load_dword v163, v[120:121], off
	global_load_dword v164, v[126:127], off
	global_load_dword v165, v[124:125], off
	global_load_dword v166, v[130:131], off
	global_load_dword v167, v[128:129], off
	global_load_dword v168, v[134:135], off
	global_load_dword v169, v[132:133], off
	global_load_dword v170, v[138:139], off
	global_load_dword v171, v[136:137], off
	global_load_dword v172, v[142:143], off
	global_load_dword v173, v[140:141], off
	s_add_i32 s27, s27, 16
	s_add_i32 s23, s23, 16
	s_add_i32 s41, s41, -16
	v_mad_u64_u32 v[110:111], s[42:43], v113, s33, v[10:11]
	s_cmp_lg_u32 s41, 0
	v_mad_u64_u32 v[114:115], s[42:43], v112, s33, v[10:11]
	v_mad_u64_u32 v[116:117], s[42:43], v145, s33, v[10:11]
	v_mad_u64_u32 v[118:119], s[42:43], v144, s33, v[10:11]
	v_mad_u64_u32 v[120:121], s[42:43], v147, s33, v[10:11]
	v_mad_u64_u32 v[122:123], s[42:43], v146, s33, v[10:11]
	v_mad_u64_u32 v[124:125], s[42:43], v149, s33, v[10:11]
	v_mad_u64_u32 v[126:127], s[42:43], v148, s33, v[10:11]
	v_mad_u64_u32 v[128:129], s[42:43], v151, s33, v[10:11]
	v_mad_u64_u32 v[130:131], s[42:43], v150, s33, v[10:11]
	v_mad_u64_u32 v[132:133], s[42:43], v153, s33, v[10:11]
	v_mad_u64_u32 v[134:135], s[42:43], v152, s33, v[10:11]
	v_mad_u64_u32 v[136:137], s[42:43], v155, s33, v[10:11]
	v_mad_u64_u32 v[138:139], s[42:43], v154, s33, v[10:11]
	v_mad_u64_u32 v[140:141], s[42:43], v157, s33, v[10:11]
	v_mad_u64_u32 v[142:143], s[42:43], v156, s33, v[10:11]
	s_waitcnt vmcnt(16)
	ds_write_b32 v6, v76
	s_waitcnt vmcnt(30)
	ds_write_b32 v32, v77
	s_waitcnt vmcnt(29)
	ds_write_b32 v34, v78
	s_waitcnt vmcnt(28)
	ds_write_b32 v36, v79
	s_waitcnt vmcnt(27)
	ds_write_b32 v38, v80
	s_waitcnt vmcnt(26)
	ds_write_b32 v40, v81
	s_waitcnt vmcnt(25)
	ds_write_b32 v42, v82
	s_waitcnt vmcnt(24)
	ds_write_b32 v44, v83
	s_waitcnt vmcnt(23)
	ds_write_b32 v46, v84
	s_waitcnt vmcnt(22)
	ds_write_b32 v48, v85
	s_waitcnt vmcnt(21)
	ds_write_b32 v50, v86
	s_waitcnt vmcnt(20)
	ds_write_b32 v52, v87
	s_waitcnt vmcnt(19)
	ds_write_b32 v54, v88
	s_waitcnt vmcnt(18)
	ds_write_b32 v56, v89
	s_waitcnt vmcnt(17)
	ds_write_b32 v58, v90
	s_waitcnt vmcnt(16)
	ds_write_b32 v60, v91
	s_waitcnt vmcnt(0)
	ds_write_b32 v110, v158
	s_waitcnt vmcnt(14)
	ds_write_b32 v114, v159
	s_waitcnt vmcnt(13)
	ds_write_b32 v116, v160
	s_waitcnt vmcnt(12)
	ds_write_b32 v118, v161
	s_waitcnt vmcnt(11)
	ds_write_b32 v120, v162
	s_waitcnt vmcnt(10)
	ds_write_b32 v122, v163
	s_waitcnt vmcnt(9)
	ds_write_b32 v124, v164
	s_waitcnt vmcnt(8)
	ds_write_b32 v126, v165
	s_waitcnt vmcnt(7)
	ds_write_b32 v128, v166
	s_waitcnt vmcnt(6)
	ds_write_b32 v130, v167
	s_waitcnt vmcnt(5)
	ds_write_b32 v132, v168
	s_waitcnt vmcnt(4)
	ds_write_b32 v134, v169
	s_waitcnt vmcnt(3)
	ds_write_b32 v136, v170
	s_waitcnt vmcnt(2)
	ds_write_b32 v138, v171
	s_waitcnt vmcnt(1)
	ds_write_b32 v140, v172
	s_waitcnt vmcnt(0)
	ds_write_b32 v142, v173

.LBB0_1186:
	s_cmp_ge_i32 s36, s28
	s_cselect_b64 s[6:7], -1, 0
	s_and_b64 s[4:5], s[6:7], s[4:5]
	s_andn2_b64 vcc, exec, s[4:5]
	s_cbranch_vccnz .LBB0_1206
	s_waitcnt lgkmcnt(0)
	v_readlane_b32 s8, v254, 0
	v_readlane_b32 s9, v255, 20
	s_nop 3
	s_cmp_lt_u32 s8, 16
	s_cbranch_scc1 .Lstg_a8_done
	s_cmp_eq_u32 s9, 3
	s_cbranch_scc1 .Lstg_a8_done
	s_mul_i32 s8, s8, 5
	s_and_b32 s8, s8, 15
	s_cmp_eq_u32 s8, 0
	s_cbranch_scc1 .Lstg_a8_done
